# gate columns and retention value rows also stored in MFMA-fragment order (free workspace at 748/780 MiB) by the in-proj epilogues; P3 gate and value fragment loads and the scan value fragment loads re
# speedup vs baseline: 1.0241x; 1.0109x over previous
;     __device__ __forceinline__ void operator()(const f32x4 (&acc)[2][2][4][2], const Unit& u, int wr, int wc, int fr, int fq) const {
;     ...
;                 const int row = row0 + ai * HALF + m * 16, pos = row & (MS - 1);
;                 const float rs = rstd[row];
; #pragma unroll
;                 for (int bj = 0; bj < 2; ++bj) {
;                     const int c0 = u.pn * BM + bj * HALF + wc * 32 + 8 * fq;
;                     f32x4 v0 = acc[ai][bj][m][0] * rs, v1 = acc[ai][bj][m][1] * rs;
;                     if (kind <= 1) {
;                         float s = (v0[0] * v0[0] + v0[1] * v0[1]) + (v0[2] * v0[2] + v0[3] * v0[3]) + (v1[0] * v1[0] + v1[1] * v1[1]) + (v1[2] * v1[2] + v1[3] * v1[3]);
;                         s += __shfl_xor(s, 16); s += __shfl_xor(s, 32);
;                         const int head = (u.pn & 3) * 2 + bj;
;                         if (fq == 0) ssq[(size_t)((kind * 8 + head) * 4 + wc) * MT + row] = s;
;                     } else if (kind <= 3) {
;                         const int i0 = (c0 & 127) >> 1;
;                         const f32x4 csa = *(const f32x4*)(cs + (size_t)pos * 64 + i0), csb = *(const f32x4*)(cs + (size_t)pos * 64 + i0 + 2);
;                         const float sc = (kind == 3) ? KSCALE : 1.0f;
;                         f32x4 w0, w1;
;                         w0[0] = (v0[0] * csa[0] - v0[1] * csa[1]) * sc; w0[1] = (v0[1] * csa[0] + v0[0] * csa[1]) * sc;
;                         w0[2] = (v0[2] * csa[2] - v0[3] * csa[3]) * sc; w0[3] = (v0[3] * csa[2] + v0[2] * csa[3]) * sc;
;                         w1[0] = (v1[0] * csb[0] - v1[1] * csb[1]) * sc; w1[1] = (v1[1] * csb[0] + v1[0] * csb[1]) * sc;
;                         w1[2] = (v1[2] * csb[2] - v1[3] * csb[3]) * sc; w1[3] = (v1[3] * csb[2] + v1[2] * csb[3]) * sc;
;                         v0 = w0; v1 = w1;
;                     } else {
; #pragma unroll
;                         for (int j = 0; j < 4; ++j) { v0[j] = v0[j] * __builtin_amdgcn_rcpf(1.0f + __builtin_amdgcn_exp2f(-1.4426950408889634f * v0[j]));
;                                                       v1[j] = v1[j] * __builtin_amdgcn_rcpf(1.0f + __builtin_amdgcn_exp2f(-1.4426950408889634f * v1[j])); }
.LBB0_226:
	s_add_i32 s100, s66, -8
	v_mov_b32_e32 v240, s100
	v_cmp_gt_u32_e64 s[100:101], 8, v240
	v_mov_b32_e32 v241, 0x2ec00000
	v_mov_b32_e32 v244, 0xe000000
	v_add_u32_e32 v245, -8, v240
	s_nop 0
	v_cndmask_b32_e64 v241, v241, v244, s[100:101]
	v_cndmask_b32_e64 v245, v245, v240, s[100:101]
	v_mov_b32_e32 v233, 11
	v_mov_b32_e32 v244, 12
	v_cndmask_b32_e64 v233, v233, v244, s[100:101]
	v_cmp_gt_u32_e64 s[100:101], 12, v240
	v_lshlrev_b32_e32 v240, 13, v245
	v_lshl_add_u32 v240, v161, 5, v240
	v_and_b32_e32 v245, 15, v159
	v_lshl_add_u32 v240, v245, 4, v240
	v_add_u32_e32 v240, v241, v240
	v_mov_b32_e32 v241, 0
	v_mov_b32_e32 v238, s62
	v_mov_b32_e32 v239, s63
	v_lshl_add_u64 v[238:239], v[238:239], 0, v[240:241]
	v_mov_b32_e32 v242, 0x100
	v_mov_b32_e32 v244, 0x1000
	v_cndmask_b32_e64 v242, v242, v244, s[100:101]
	v_mov_b32_e32 v243, 0
	v_lshl_add_u32 v142, s38, 8, v159
	v_readlane_b32 s56, v250, 22
	v_ashrrev_i32_e32 v143, 31, v142
	v_readlane_b32 s57, v250, 23
	s_ashr_i32 s4, s66, 2
	s_cmp_gt_i32 s4, 1
	v_lshl_add_u64 v[146:147], v[142:143], 2, s[56:57]
	global_load_dword v148, v[146:147], off
	global_load_dword v226, v[146:147], off offset:64
	global_load_dword v227, v[146:147], off offset:128
	global_load_dword v228, v[146:147], off offset:192
	global_load_dword v229, v[146:147], off offset:512
	global_load_dword v230, v[146:147], off offset:576
	global_load_dword v231, v[146:147], off offset:640
	global_load_dword v232, v[146:147], off offset:704
	s_cselect_b64 s[0:1], -1, 0
	s_cmp_gt_u32 s4, 3
	s_cselect_b64 s[8:9], -1, 0
	s_cmp_eq_u32 s4, 3
	v_lshlrev_b32_e32 v149, 6, v142
	s_cselect_b64 vcc, -1, 0
	v_and_b32_e32 v163, 0x1f3c0, v149
	v_cndmask_b32_e32 v144, 1.0, v220, vcc
	s_mov_b64 s[2:3], -1
	s_and_b64 vcc, exec, s[0:1]
	s_waitcnt vmcnt(0)
	v_pk_mul_f32 v[126:127], v[126:127], v[148:149] op_sel_hi:[1,0]
	v_pk_mul_f32 v[124:125], v[124:125], v[148:149] op_sel_hi:[1,0]
	v_pk_mul_f32 v[122:123], v[122:123], v[148:149] op_sel_hi:[1,0]
	v_pk_mul_f32 v[120:121], v[120:121], v[148:149] op_sel_hi:[1,0]
	v_cndmask_b32_e64 v149, 0, 1, s[8:9]
	v_cmp_ne_u32_e64 s[38:39], 1, v149
	s_cbranch_vccz .LBB0_232
	s_and_b64 vcc, exec, s[38:39]
	s_cbranch_vccnz .LBB0_229
	v_mul_f32_e32 v149, 0xbfb8aa3b, v124
	v_exp_f32_e32 v149, v149
	v_mul_f32_e32 v150, 0xbfb8aa3b, v120
	v_mul_f32_e32 v151, 0xbfb8aa3b, v125
	v_exp_f32_e32 v152, v150
	v_exp_f32_e32 v151, v151
	v_add_f32_e32 v149, 1.0, v149
	v_rcp_f32_e32 v150, v149
	v_add_f32_e32 v149, 1.0, v152
	v_rcp_f32_e32 v154, v149
	v_add_f32_e32 v149, 1.0, v151
	v_mul_f32_e32 v153, 0xbfb8aa3b, v122
	v_rcp_f32_e32 v151, v149
	v_mul_f32_e32 v149, 0xbfb8aa3b, v121
	v_mul_f32_e32 v152, 0xbfb8aa3b, v126
	v_exp_f32_e32 v153, v153
	v_mul_f32_e32 v155, 0xbfb8aa3b, v127
	v_mul_f32_e32 v156, 0xbfb8aa3b, v123
	v_exp_f32_e32 v149, v149
	v_exp_f32_e32 v152, v152
	v_exp_f32_e32 v155, v155
	v_exp_f32_e32 v157, v156
	v_add_f32_e32 v153, 1.0, v153
	v_add_f32_e32 v149, 1.0, v149
	v_add_f32_e32 v152, 1.0, v152
	v_rcp_f32_e32 v156, v153
	v_add_f32_e32 v153, 1.0, v155
	v_add_f32_e32 v155, 1.0, v157
	v_rcp_f32_e32 v152, v152
	v_rcp_f32_e32 v153, v153
	v_rcp_f32_e32 v157, v155
	v_rcp_f32_e32 v155, v149
	v_pk_mul_f32 v[150:151], v[124:125], v[150:151]
	v_pk_mul_f32 v[152:153], v[126:127], v[152:153]
	v_pk_mul_f32 v[156:157], v[122:123], v[156:157]
	v_pk_mul_f32 v[154:155], v[120:121], v[154:155]
	s_mov_b64 s[2:3], 0

; __device__ __forceinline__ unsigned cvt_pk_bf16(float lo, float hi) { unsigned r; asm volatile("v_cvt_pk_bf16_f32 %0, %1, %2" : "=v"(r) : "v"(lo), "v"(hi)); return r; }
;     __device__ __forceinline__ void operator()(const f32x4 (&acc)[2][2][4][2], const Unit& u, int wr, int wc, int fr, int fq) const {
;     ...
;                     f32x4 v0 = acc[ai][bj][m][0] * rs, v1 = acc[ai][bj][m][1] * rs;
;                     if (kind <= 1) {
;                         float s = (v0[0] * v0[0] + v0[1] * v0[1]) + (v0[2] * v0[2] + v0[3] * v0[3]) + (v1[0] * v1[0] + v1[1] * v1[1]) + (v1[2] * v1[2] + v1[3] * v1[3]);
;                         s += __shfl_xor(s, 16); s += __shfl_xor(s, 32);
;                         const int head = (u.pn & 3) * 2 + bj;
;                         if (fq == 0) ssq[(size_t)((kind * 8 + head) * 4 + wc) * MT + row] = s;
;                     } else if (kind <= 3) {
;                         const int i0 = (c0 & 127) >> 1;
;                         const f32x4 csa = *(const f32x4*)(cs + (size_t)pos * 64 + i0), csb = *(const f32x4*)(cs + (size_t)pos * 64 + i0 + 2);
;                         const float sc = (kind == 3) ? KSCALE : 1.0f;
;                         f32x4 w0, w1;
;                         w0[0] = (v0[0] * csa[0] - v0[1] * csa[1]) * sc; w0[1] = (v0[1] * csa[0] + v0[0] * csa[1]) * sc;
;                         w0[2] = (v0[2] * csa[2] - v0[3] * csa[3]) * sc; w0[3] = (v0[3] * csa[2] + v0[2] * csa[3]) * sc;
;                         w1[0] = (v1[0] * csb[0] - v1[1] * csb[1]) * sc; w1[1] = (v1[1] * csb[0] + v1[0] * csb[1]) * sc;
;                         w1[2] = (v1[2] * csb[2] - v1[3] * csb[3]) * sc; w1[3] = (v1[3] * csb[2] + v1[2] * csb[3]) * sc;
;                         v0 = w0; v1 = w1;
;                     } else {
; #pragma unroll
;                         for (int j = 0; j < 4; ++j) { v0[j] = v0[j] * __builtin_amdgcn_rcpf(1.0f + __builtin_amdgcn_exp2f(-1.4426950408889634f * v0[j]));
;                                                       v1[j] = v1[j] * __builtin_amdgcn_rcpf(1.0f + __builtin_amdgcn_exp2f(-1.4426950408889634f * v1[j])); }
;                     }
;                     u32x4 w; w.x = cvt_pk_bf16(v0[0], v0[1]); w.y = cvt_pk_bf16(v0[2], v0[3]); w.z = cvt_pk_bf16(v1[0], v1[1]); w.w = cvt_pk_bf16(v1[2], v1[3]);
;                     *(u32x4*)(O + (size_t)row * TOKP + c0) = w;
.LBB0_236:
	v_lshl_or_b32 v120, s66, 8, v161
	v_mov_b64_e32 v[122:123], s[80:81]
	s_movk_i32 s2, 0x2900
	v_mad_i64_i32 v[122:123], s[2:3], v142, s2, v[122:123]
	v_ashrrev_i32_e32 v121, 31, v120
	v_cvt_pk_bf16_f32 v124, v150, v151
	v_cvt_pk_bf16_f32 v125, v152, v153
	v_lshl_add_u64 v[122:123], v[120:121], 1, v[122:123]
	v_cvt_pk_bf16_f32 v126, v154, v155
	v_cvt_pk_bf16_f32 v127, v156, v157
	v_and_b32_e32 v244, -16, v142
	v_lshlrev_b32_e32 v244, v233, v244
	v_mov_b32_e32 v245, 0
	v_lshl_add_u64 v[246:247], v[244:245], 0, v[238:239]
	v_cndmask_b32_e64 v246, v122, v246, s[100:101]
	v_cndmask_b32_e64 v247, v123, v247, s[100:101]
	v_lshl_add_u64 v[248:249], v[246:247], 0, v[242:243]
	global_store_dwordx4 v[246:247], v[124:127], off
	v_mov_b32_e32 v149, v148
	v_pk_mul_f32 v[116:117], v[116:117], v[148:149]
	v_mov_b32_e32 v124, v148
	v_mov_b32_e32 v125, v148
	v_pk_mul_f32 v[118:119], v[118:119], v[124:125]
	v_pk_mul_f32 v[114:115], v[114:115], v[124:125]
	v_cndmask_b32_e64 v124, 0, 1, s[0:1]
	v_pk_mul_f32 v[112:113], v[112:113], v[148:149]
	v_cmp_ne_u32_e64 s[40:41], 1, v124
	s_andn2_b64 vcc, exec, s[0:1]
	s_mov_b64 s[0:1], -1
	s_cbranch_vccnz .LBB0_242
	s_and_b64 vcc, exec, s[38:39]
	s_cbranch_vccnz .LBB0_239
	v_mul_f32_e32 v125, 0xbfb8aa3b, v112
	v_mul_f32_e32 v126, 0xbfb8aa3b, v117
	v_exp_f32_e32 v125, v125
	v_exp_f32_e32 v126, v126
	v_mul_f32_e32 v127, 0xbfb8aa3b, v118
	v_mul_f32_e32 v149, 0xbfb8aa3b, v114
	v_add_f32_e32 v125, 1.0, v125
	v_rcp_f32_e32 v148, v125
	v_add_f32_e32 v125, 1.0, v126
	v_mul_f32_e32 v126, 0xbfb8aa3b, v113
	v_exp_f32_e32 v126, v126
	v_exp_f32_e32 v127, v127
	v_exp_f32_e32 v149, v149
	v_mul_f32_e32 v124, 0xbfb8aa3b, v116
	v_add_f32_e32 v152, 1.0, v126
	v_add_f32_e32 v126, 1.0, v127
	v_add_f32_e32 v127, 1.0, v149
	v_mul_f32_e32 v149, 0xbfb8aa3b, v119
	v_mul_f32_e32 v150, 0xbfb8aa3b, v115
	v_exp_f32_e32 v124, v124
	v_exp_f32_e32 v149, v149
	v_exp_f32_e32 v151, v150
	v_rcp_f32_e32 v150, v127
	v_add_f32_e32 v124, 1.0, v124
	v_add_f32_e32 v127, 1.0, v149
	v_add_f32_e32 v149, 1.0, v151
	v_rcp_f32_e32 v124, v124
	v_rcp_f32_e32 v125, v125
	v_rcp_f32_e32 v126, v126
	v_rcp_f32_e32 v127, v127
	v_rcp_f32_e32 v151, v149
	v_rcp_f32_e32 v149, v152
	v_pk_mul_f32 v[124:125], v[116:117], v[124:125]
	v_pk_mul_f32 v[126:127], v[118:119], v[126:127]
	v_pk_mul_f32 v[150:151], v[114:115], v[150:151]
	v_pk_mul_f32 v[148:149], v[112:113], v[148:149]
	s_mov_b64 s[0:1], 0

; __device__ __forceinline__ unsigned cvt_pk_bf16(float lo, float hi) { unsigned r; asm volatile("v_cvt_pk_bf16_f32 %0, %1, %2" : "=v"(r) : "v"(lo), "v"(hi)); return r; }
;     __device__ __forceinline__ void operator()(const f32x4 (&acc)[2][2][4][2], const Unit& u, int wr, int wc, int fr, int fq) const {
;     ...
;                     f32x4 v0 = acc[ai][bj][m][0] * rs, v1 = acc[ai][bj][m][1] * rs;
;                     if (kind <= 1) {
;                         float s = (v0[0] * v0[0] + v0[1] * v0[1]) + (v0[2] * v0[2] + v0[3] * v0[3]) + (v1[0] * v1[0] + v1[1] * v1[1]) + (v1[2] * v1[2] + v1[3] * v1[3]);
;                         s += __shfl_xor(s, 16); s += __shfl_xor(s, 32);
;                         const int head = (u.pn & 3) * 2 + bj;
;                         if (fq == 0) ssq[(size_t)((kind * 8 + head) * 4 + wc) * MT + row] = s;
;                     } else if (kind <= 3) {
;                         const int i0 = (c0 & 127) >> 1;
;                         const f32x4 csa = *(const f32x4*)(cs + (size_t)pos * 64 + i0), csb = *(const f32x4*)(cs + (size_t)pos * 64 + i0 + 2);
;                         const float sc = (kind == 3) ? KSCALE : 1.0f;
;                         f32x4 w0, w1;
;                         w0[0] = (v0[0] * csa[0] - v0[1] * csa[1]) * sc; w0[1] = (v0[1] * csa[0] + v0[0] * csa[1]) * sc;
;                         w0[2] = (v0[2] * csa[2] - v0[3] * csa[3]) * sc; w0[3] = (v0[3] * csa[2] + v0[2] * csa[3]) * sc;
;                         w1[0] = (v1[0] * csb[0] - v1[1] * csb[1]) * sc; w1[1] = (v1[1] * csb[0] + v1[0] * csb[1]) * sc;
;                         w1[2] = (v1[2] * csb[2] - v1[3] * csb[3]) * sc; w1[3] = (v1[3] * csb[2] + v1[2] * csb[3]) * sc;
;                         v0 = w0; v1 = w1;
;                     } else {
; #pragma unroll
;                         for (int j = 0; j < 4; ++j) { v0[j] = v0[j] * __builtin_amdgcn_rcpf(1.0f + __builtin_amdgcn_exp2f(-1.4426950408889634f * v0[j]));
;                                                       v1[j] = v1[j] * __builtin_amdgcn_rcpf(1.0f + __builtin_amdgcn_exp2f(-1.4426950408889634f * v1[j])); }
;                     }
;                     u32x4 w; w.x = cvt_pk_bf16(v0[0], v0[1]); w.y = cvt_pk_bf16(v0[2], v0[3]); w.z = cvt_pk_bf16(v1[0], v1[1]); w.w = cvt_pk_bf16(v1[2], v1[3]);
;                     *(u32x4*)(O + (size_t)row * TOKP + c0) = w;
.LBB0_256:
	v_mov_b64_e32 v[104:105], s[80:81]
	s_movk_i32 s0, 0x2900
	v_mad_i64_i32 v[104:105], s[0:1], v114, s0, v[104:105]
	v_cvt_pk_bf16_f32 v106, v116, v117
	v_cvt_pk_bf16_f32 v107, v118, v119
	v_lshl_add_u64 v[104:105], v[120:121], 1, v[104:105]
	v_mov_b32_e32 v113, v112
	v_cvt_pk_bf16_f32 v108, v122, v123
	v_cvt_pk_bf16_f32 v109, v124, v125
	v_and_b32_e32 v244, -16, v114
	v_lshlrev_b32_e32 v244, v233, v244
	v_mov_b32_e32 v245, 0
	v_lshl_add_u64 v[246:247], v[244:245], 0, v[238:239]
	v_cndmask_b32_e64 v246, v104, v246, s[100:101]
	v_cndmask_b32_e64 v247, v105, v247, s[100:101]
	v_lshl_add_u64 v[248:249], v[246:247], 0, v[242:243]
	global_store_dwordx4 v[246:247], v[106:109], off
	v_pk_mul_f32 v[100:101], v[100:101], v[112:113]
	v_pk_mul_f32 v[96:97], v[96:97], v[112:113]
	v_mov_b32_e32 v106, v112
	v_mov_b32_e32 v107, v112
	v_pk_mul_f32 v[102:103], v[102:103], v[106:107]
	v_pk_mul_f32 v[98:99], v[98:99], v[106:107]
	s_and_b64 vcc, exec, s[40:41]
	s_mov_b64 s[0:1], -1
	s_cbranch_vccnz .LBB0_262
	s_and_b64 vcc, exec, s[38:39]
	s_cbranch_vccnz .LBB0_259
	v_mul_f32_e32 v107, 0xbfb8aa3b, v96
	v_mul_f32_e32 v108, 0xbfb8aa3b, v101
	v_exp_f32_e32 v107, v107
	v_exp_f32_e32 v108, v108
	v_mul_f32_e32 v109, 0xbfb8aa3b, v102
	v_mul_f32_e32 v111, 0xbfb8aa3b, v98
	v_add_f32_e32 v107, 1.0, v107
	v_rcp_f32_e32 v110, v107
	v_add_f32_e32 v107, 1.0, v108
	v_mul_f32_e32 v108, 0xbfb8aa3b, v97
	v_exp_f32_e32 v108, v108
	v_exp_f32_e32 v109, v109
	v_exp_f32_e32 v111, v111
	v_mul_f32_e32 v106, 0xbfb8aa3b, v100
	v_add_f32_e32 v114, 1.0, v108
	v_add_f32_e32 v108, 1.0, v109
	v_add_f32_e32 v109, 1.0, v111
	v_mul_f32_e32 v111, 0xbfb8aa3b, v103
	v_mul_f32_e32 v112, 0xbfb8aa3b, v99
	v_exp_f32_e32 v106, v106
	v_exp_f32_e32 v111, v111
	v_exp_f32_e32 v113, v112
	v_rcp_f32_e32 v112, v109
	v_add_f32_e32 v106, 1.0, v106
	v_add_f32_e32 v109, 1.0, v111
	v_add_f32_e32 v111, 1.0, v113
	v_rcp_f32_e32 v106, v106
	v_rcp_f32_e32 v107, v107
	v_rcp_f32_e32 v108, v108
	v_rcp_f32_e32 v109, v109
	v_rcp_f32_e32 v113, v111
	v_rcp_f32_e32 v111, v114
	v_pk_mul_f32 v[106:107], v[100:101], v[106:107]
	v_pk_mul_f32 v[108:109], v[102:103], v[108:109]
	v_pk_mul_f32 v[112:113], v[98:99], v[112:113]
	v_pk_mul_f32 v[110:111], v[96:97], v[110:111]
	s_mov_b64 s[0:1], 0

; __device__ __forceinline__ unsigned cvt_pk_bf16(float lo, float hi) { unsigned r; asm volatile("v_cvt_pk_bf16_f32 %0, %1, %2" : "=v"(r) : "v"(lo), "v"(hi)); return r; }
;     __device__ __forceinline__ void operator()(const f32x4 (&acc)[2][2][4][2], const Unit& u, int wr, int wc, int fr, int fq) const {
;     ...
;                     f32x4 v0 = acc[ai][bj][m][0] * rs, v1 = acc[ai][bj][m][1] * rs;
;                     if (kind <= 1) {
;                         float s = (v0[0] * v0[0] + v0[1] * v0[1]) + (v0[2] * v0[2] + v0[3] * v0[3]) + (v1[0] * v1[0] + v1[1] * v1[1]) + (v1[2] * v1[2] + v1[3] * v1[3]);
;                         s += __shfl_xor(s, 16); s += __shfl_xor(s, 32);
;                         const int head = (u.pn & 3) * 2 + bj;
;                         if (fq == 0) ssq[(size_t)((kind * 8 + head) * 4 + wc) * MT + row] = s;
;                     } else if (kind <= 3) {
;                         const int i0 = (c0 & 127) >> 1;
;                         const f32x4 csa = *(const f32x4*)(cs + (size_t)pos * 64 + i0), csb = *(const f32x4*)(cs + (size_t)pos * 64 + i0 + 2);
;                         const float sc = (kind == 3) ? KSCALE : 1.0f;
;                         f32x4 w0, w1;
;                         w0[0] = (v0[0] * csa[0] - v0[1] * csa[1]) * sc; w0[1] = (v0[1] * csa[0] + v0[0] * csa[1]) * sc;
;                         w0[2] = (v0[2] * csa[2] - v0[3] * csa[3]) * sc; w0[3] = (v0[3] * csa[2] + v0[2] * csa[3]) * sc;
;                         w1[0] = (v1[0] * csb[0] - v1[1] * csb[1]) * sc; w1[1] = (v1[1] * csb[0] + v1[0] * csb[1]) * sc;
;                         w1[2] = (v1[2] * csb[2] - v1[3] * csb[3]) * sc; w1[3] = (v1[3] * csb[2] + v1[2] * csb[3]) * sc;
;                         v0 = w0; v1 = w1;
;                     } else {
; #pragma unroll
;                         for (int j = 0; j < 4; ++j) { v0[j] = v0[j] * __builtin_amdgcn_rcpf(1.0f + __builtin_amdgcn_exp2f(-1.4426950408889634f * v0[j]));
;                                                       v1[j] = v1[j] * __builtin_amdgcn_rcpf(1.0f + __builtin_amdgcn_exp2f(-1.4426950408889634f * v1[j])); }
;                     }
;                     u32x4 w; w.x = cvt_pk_bf16(v0[0], v0[1]); w.y = cvt_pk_bf16(v0[2], v0[3]); w.z = cvt_pk_bf16(v1[0], v1[1]); w.w = cvt_pk_bf16(v1[2], v1[3]);
;                     *(u32x4*)(O + (size_t)row * TOKP + c0) = w;
.LBB0_276:
	v_mov_b64_e32 v[88:89], s[80:81]
	s_movk_i32 s0, 0x2900
	v_mad_i64_i32 v[88:89], s[0:1], v98, s0, v[88:89]
	v_cvt_pk_bf16_f32 v90, v100, v101
	v_cvt_pk_bf16_f32 v91, v102, v103
	v_lshl_add_u64 v[88:89], v[120:121], 1, v[88:89]
	v_mov_b32_e32 v97, v96
	v_cvt_pk_bf16_f32 v92, v104, v105
	v_cvt_pk_bf16_f32 v93, v106, v107
	v_and_b32_e32 v244, -16, v98
	v_lshlrev_b32_e32 v244, v233, v244
	v_mov_b32_e32 v245, 0
	v_lshl_add_u64 v[246:247], v[244:245], 0, v[238:239]
	v_cndmask_b32_e64 v246, v88, v246, s[100:101]
	v_cndmask_b32_e64 v247, v89, v247, s[100:101]
	v_lshl_add_u64 v[248:249], v[246:247], 0, v[242:243]
	global_store_dwordx4 v[246:247], v[90:93], off
	v_pk_mul_f32 v[84:85], v[84:85], v[96:97]
	v_pk_mul_f32 v[80:81], v[80:81], v[96:97]
	v_mov_b32_e32 v90, v96
	v_mov_b32_e32 v91, v96
	v_pk_mul_f32 v[86:87], v[86:87], v[90:91]
	v_pk_mul_f32 v[82:83], v[82:83], v[90:91]
	s_and_b64 vcc, exec, s[40:41]
	s_mov_b64 s[0:1], -1
	s_cbranch_vccnz .LBB0_282
	s_and_b64 vcc, exec, s[38:39]
	s_cbranch_vccnz .LBB0_279
	v_mul_f32_e32 v91, 0xbfb8aa3b, v80
	v_mul_f32_e32 v92, 0xbfb8aa3b, v85
	v_exp_f32_e32 v91, v91
	v_exp_f32_e32 v92, v92
	v_mul_f32_e32 v93, 0xbfb8aa3b, v86
	v_mul_f32_e32 v95, 0xbfb8aa3b, v82
	v_add_f32_e32 v91, 1.0, v91
	v_rcp_f32_e32 v94, v91
	v_add_f32_e32 v91, 1.0, v92
	v_mul_f32_e32 v92, 0xbfb8aa3b, v81
	v_exp_f32_e32 v92, v92
	v_exp_f32_e32 v93, v93
	v_exp_f32_e32 v95, v95
	v_mul_f32_e32 v90, 0xbfb8aa3b, v84
	v_add_f32_e32 v98, 1.0, v92
	v_add_f32_e32 v92, 1.0, v93
	v_add_f32_e32 v93, 1.0, v95
	v_mul_f32_e32 v95, 0xbfb8aa3b, v87
	v_mul_f32_e32 v96, 0xbfb8aa3b, v83
	v_exp_f32_e32 v90, v90
	v_exp_f32_e32 v95, v95
	v_exp_f32_e32 v97, v96
	v_rcp_f32_e32 v96, v93
	v_add_f32_e32 v90, 1.0, v90
	v_add_f32_e32 v93, 1.0, v95
	v_add_f32_e32 v95, 1.0, v97
	v_rcp_f32_e32 v90, v90
	v_rcp_f32_e32 v91, v91
	v_rcp_f32_e32 v92, v92
	v_rcp_f32_e32 v93, v93
	v_rcp_f32_e32 v97, v95
	v_rcp_f32_e32 v95, v98
	v_pk_mul_f32 v[90:91], v[84:85], v[90:91]
	v_pk_mul_f32 v[92:93], v[86:87], v[92:93]
	v_pk_mul_f32 v[96:97], v[82:83], v[96:97]
	v_pk_mul_f32 v[94:95], v[80:81], v[94:95]
	s_mov_b64 s[0:1], 0

; __device__ __forceinline__ unsigned cvt_pk_bf16(float lo, float hi) { unsigned r; asm volatile("v_cvt_pk_bf16_f32 %0, %1, %2" : "=v"(r) : "v"(lo), "v"(hi)); return r; }
;     __device__ __forceinline__ void operator()(const f32x4 (&acc)[2][2][4][2], const Unit& u, int wr, int wc, int fr, int fq) const {
;     ...
;                     f32x4 v0 = acc[ai][bj][m][0] * rs, v1 = acc[ai][bj][m][1] * rs;
;                     if (kind <= 1) {
;                         float s = (v0[0] * v0[0] + v0[1] * v0[1]) + (v0[2] * v0[2] + v0[3] * v0[3]) + (v1[0] * v1[0] + v1[1] * v1[1]) + (v1[2] * v1[2] + v1[3] * v1[3]);
;                         s += __shfl_xor(s, 16); s += __shfl_xor(s, 32);
;                         const int head = (u.pn & 3) * 2 + bj;
;                         if (fq == 0) ssq[(size_t)((kind * 8 + head) * 4 + wc) * MT + row] = s;
;                     } else if (kind <= 3) {
;                         const int i0 = (c0 & 127) >> 1;
;                         const f32x4 csa = *(const f32x4*)(cs + (size_t)pos * 64 + i0), csb = *(const f32x4*)(cs + (size_t)pos * 64 + i0 + 2);
;                         const float sc = (kind == 3) ? KSCALE : 1.0f;
;                         f32x4 w0, w1;
;                         w0[0] = (v0[0] * csa[0] - v0[1] * csa[1]) * sc; w0[1] = (v0[1] * csa[0] + v0[0] * csa[1]) * sc;
;                         w0[2] = (v0[2] * csa[2] - v0[3] * csa[3]) * sc; w0[3] = (v0[3] * csa[2] + v0[2] * csa[3]) * sc;
;                         w1[0] = (v1[0] * csb[0] - v1[1] * csb[1]) * sc; w1[1] = (v1[1] * csb[0] + v1[0] * csb[1]) * sc;
;                         w1[2] = (v1[2] * csb[2] - v1[3] * csb[3]) * sc; w1[3] = (v1[3] * csb[2] + v1[2] * csb[3]) * sc;
;                         v0 = w0; v1 = w1;
;                     } else {
; #pragma unroll
;                         for (int j = 0; j < 4; ++j) { v0[j] = v0[j] * __builtin_amdgcn_rcpf(1.0f + __builtin_amdgcn_exp2f(-1.4426950408889634f * v0[j]));
;                                                       v1[j] = v1[j] * __builtin_amdgcn_rcpf(1.0f + __builtin_amdgcn_exp2f(-1.4426950408889634f * v1[j])); }
;                     }
;                     u32x4 w; w.x = cvt_pk_bf16(v0[0], v0[1]); w.y = cvt_pk_bf16(v0[2], v0[3]); w.z = cvt_pk_bf16(v1[0], v1[1]); w.w = cvt_pk_bf16(v1[2], v1[3]);
;                     *(u32x4*)(O + (size_t)row * TOKP + c0) = w;
.LBB0_296:
	v_mov_b64_e32 v[72:73], s[80:81]
	s_movk_i32 s0, 0x2900
	v_mad_i64_i32 v[72:73], s[0:1], v82, s0, v[72:73]
	v_cvt_pk_bf16_f32 v74, v84, v85
	v_cvt_pk_bf16_f32 v75, v86, v87
	v_lshl_add_u64 v[72:73], v[120:121], 1, v[72:73]
	v_mov_b32_e32 v81, v80
	v_cvt_pk_bf16_f32 v76, v88, v89
	v_cvt_pk_bf16_f32 v77, v90, v91
	v_and_b32_e32 v244, -16, v82
	v_lshlrev_b32_e32 v244, v233, v244
	v_mov_b32_e32 v245, 0
	v_lshl_add_u64 v[246:247], v[244:245], 0, v[238:239]
	v_cndmask_b32_e64 v246, v72, v246, s[100:101]
	v_cndmask_b32_e64 v247, v73, v247, s[100:101]
	v_lshl_add_u64 v[248:249], v[246:247], 0, v[242:243]
	global_store_dwordx4 v[246:247], v[74:77], off
	v_pk_mul_f32 v[68:69], v[68:69], v[80:81]
	v_pk_mul_f32 v[64:65], v[64:65], v[80:81]
	v_mov_b32_e32 v74, v80
	v_mov_b32_e32 v75, v80
	v_pk_mul_f32 v[70:71], v[70:71], v[74:75]
	v_pk_mul_f32 v[66:67], v[66:67], v[74:75]
	s_and_b64 vcc, exec, s[40:41]
	s_mov_b64 s[0:1], -1
	s_cbranch_vccnz .LBB0_302
	s_and_b64 vcc, exec, s[38:39]
	s_cbranch_vccnz .LBB0_299
	v_mul_f32_e32 v75, 0xbfb8aa3b, v64
	v_mul_f32_e32 v76, 0xbfb8aa3b, v69
	v_exp_f32_e32 v75, v75
	v_exp_f32_e32 v76, v76
	v_mul_f32_e32 v77, 0xbfb8aa3b, v70
	v_mul_f32_e32 v79, 0xbfb8aa3b, v66
	v_add_f32_e32 v75, 1.0, v75
	v_rcp_f32_e32 v78, v75
	v_add_f32_e32 v75, 1.0, v76
	v_mul_f32_e32 v76, 0xbfb8aa3b, v65
	v_exp_f32_e32 v76, v76
	v_exp_f32_e32 v77, v77
	v_exp_f32_e32 v79, v79
	v_mul_f32_e32 v74, 0xbfb8aa3b, v68
	v_add_f32_e32 v82, 1.0, v76
	v_add_f32_e32 v76, 1.0, v77
	v_add_f32_e32 v77, 1.0, v79
	v_mul_f32_e32 v79, 0xbfb8aa3b, v71
	v_mul_f32_e32 v80, 0xbfb8aa3b, v67
	v_exp_f32_e32 v74, v74
	v_exp_f32_e32 v79, v79
	v_exp_f32_e32 v81, v80
	v_rcp_f32_e32 v80, v77
	v_add_f32_e32 v74, 1.0, v74
	v_add_f32_e32 v77, 1.0, v79
	v_add_f32_e32 v79, 1.0, v81
	v_rcp_f32_e32 v74, v74
	v_rcp_f32_e32 v75, v75
	v_rcp_f32_e32 v76, v76
	v_rcp_f32_e32 v77, v77
	v_rcp_f32_e32 v81, v79
	v_rcp_f32_e32 v79, v82
	v_pk_mul_f32 v[74:75], v[68:69], v[74:75]
	v_pk_mul_f32 v[76:77], v[70:71], v[76:77]
	v_pk_mul_f32 v[80:81], v[66:67], v[80:81]
	v_pk_mul_f32 v[78:79], v[64:65], v[78:79]
	s_mov_b64 s[0:1], 0

; __device__ __forceinline__ unsigned cvt_pk_bf16(float lo, float hi) { unsigned r; asm volatile("v_cvt_pk_bf16_f32 %0, %1, %2" : "=v"(r) : "v"(lo), "v"(hi)); return r; }
;     __device__ __forceinline__ void operator()(const f32x4 (&acc)[2][2][4][2], const Unit& u, int wr, int wc, int fr, int fq) const {
;     ...
;                     f32x4 v0 = acc[ai][bj][m][0] * rs, v1 = acc[ai][bj][m][1] * rs;
;                     if (kind <= 1) {
;                         float s = (v0[0] * v0[0] + v0[1] * v0[1]) + (v0[2] * v0[2] + v0[3] * v0[3]) + (v1[0] * v1[0] + v1[1] * v1[1]) + (v1[2] * v1[2] + v1[3] * v1[3]);
;                         s += __shfl_xor(s, 16); s += __shfl_xor(s, 32);
;                         const int head = (u.pn & 3) * 2 + bj;
;                         if (fq == 0) ssq[(size_t)((kind * 8 + head) * 4 + wc) * MT + row] = s;
;                     } else if (kind <= 3) {
;                         const int i0 = (c0 & 127) >> 1;
;                         const f32x4 csa = *(const f32x4*)(cs + (size_t)pos * 64 + i0), csb = *(const f32x4*)(cs + (size_t)pos * 64 + i0 + 2);
;                         const float sc = (kind == 3) ? KSCALE : 1.0f;
;                         f32x4 w0, w1;
;                         w0[0] = (v0[0] * csa[0] - v0[1] * csa[1]) * sc; w0[1] = (v0[1] * csa[0] + v0[0] * csa[1]) * sc;
;                         w0[2] = (v0[2] * csa[2] - v0[3] * csa[3]) * sc; w0[3] = (v0[3] * csa[2] + v0[2] * csa[3]) * sc;
;                         w1[0] = (v1[0] * csb[0] - v1[1] * csb[1]) * sc; w1[1] = (v1[1] * csb[0] + v1[0] * csb[1]) * sc;
;                         w1[2] = (v1[2] * csb[2] - v1[3] * csb[3]) * sc; w1[3] = (v1[3] * csb[2] + v1[2] * csb[3]) * sc;
;                         v0 = w0; v1 = w1;
;                     } else {
; #pragma unroll
;                         for (int j = 0; j < 4; ++j) { v0[j] = v0[j] * __builtin_amdgcn_rcpf(1.0f + __builtin_amdgcn_exp2f(-1.4426950408889634f * v0[j]));
;                                                       v1[j] = v1[j] * __builtin_amdgcn_rcpf(1.0f + __builtin_amdgcn_exp2f(-1.4426950408889634f * v1[j])); }
;                     }
;                     u32x4 w; w.x = cvt_pk_bf16(v0[0], v0[1]); w.y = cvt_pk_bf16(v0[2], v0[3]); w.z = cvt_pk_bf16(v1[0], v1[1]); w.w = cvt_pk_bf16(v1[2], v1[3]);
;                     *(u32x4*)(O + (size_t)row * TOKP + c0) = w;
.LBB0_316:
	v_mov_b64_e32 v[56:57], s[80:81]
	s_movk_i32 s0, 0x2900
	v_mad_i64_i32 v[56:57], s[0:1], v75, s0, v[56:57]
	v_cvt_pk_bf16_f32 v58, v66, v67
	v_cvt_pk_bf16_f32 v59, v68, v69
	v_lshl_add_u64 v[56:57], v[120:121], 1, v[56:57]
	v_mov_b32_e32 v65, v64
	v_cvt_pk_bf16_f32 v60, v70, v71
	v_cvt_pk_bf16_f32 v61, v72, v73
	v_and_b32_e32 v244, -16, v75
	v_lshlrev_b32_e32 v244, v233, v244
	v_mov_b32_e32 v245, 0
	v_lshl_add_u64 v[246:247], v[244:245], 0, v[238:239]
	v_cndmask_b32_e64 v246, v56, v246, s[100:101]
	v_cndmask_b32_e64 v247, v57, v247, s[100:101]
	v_lshl_add_u64 v[248:249], v[246:247], 0, v[242:243]
	global_store_dwordx4 v[246:247], v[58:61], off
	v_pk_mul_f32 v[52:53], v[52:53], v[64:65]
	v_pk_mul_f32 v[48:49], v[48:49], v[64:65]
	v_mov_b32_e32 v58, v64
	v_mov_b32_e32 v59, v64
	v_pk_mul_f32 v[54:55], v[54:55], v[58:59]
	v_pk_mul_f32 v[50:51], v[50:51], v[58:59]
	s_and_b64 vcc, exec, s[40:41]
	s_mov_b64 s[0:1], -1
	s_cbranch_vccnz .LBB0_322
	s_and_b64 vcc, exec, s[38:39]
	s_cbranch_vccnz .LBB0_319
	v_mul_f32_e32 v59, 0xbfb8aa3b, v48
	v_mul_f32_e32 v60, 0xbfb8aa3b, v53
	v_exp_f32_e32 v59, v59
	v_exp_f32_e32 v60, v60
	v_mul_f32_e32 v61, 0xbfb8aa3b, v54
	v_mul_f32_e32 v63, 0xbfb8aa3b, v50
	v_add_f32_e32 v59, 1.0, v59
	v_rcp_f32_e32 v62, v59
	v_add_f32_e32 v59, 1.0, v60
	v_mul_f32_e32 v60, 0xbfb8aa3b, v49
	v_exp_f32_e32 v60, v60
	v_exp_f32_e32 v61, v61
	v_exp_f32_e32 v63, v63
	v_mul_f32_e32 v58, 0xbfb8aa3b, v52
	v_add_f32_e32 v66, 1.0, v60
	v_add_f32_e32 v60, 1.0, v61
	v_add_f32_e32 v61, 1.0, v63
	v_mul_f32_e32 v63, 0xbfb8aa3b, v55
	v_mul_f32_e32 v64, 0xbfb8aa3b, v51
	v_exp_f32_e32 v58, v58
	v_exp_f32_e32 v63, v63
	v_exp_f32_e32 v65, v64
	v_rcp_f32_e32 v64, v61
	v_add_f32_e32 v58, 1.0, v58
	v_add_f32_e32 v61, 1.0, v63
	v_add_f32_e32 v63, 1.0, v65
	v_rcp_f32_e32 v58, v58
	v_rcp_f32_e32 v59, v59
	v_rcp_f32_e32 v60, v60
	v_rcp_f32_e32 v61, v61
	v_rcp_f32_e32 v65, v63
	v_rcp_f32_e32 v63, v66
	v_pk_mul_f32 v[58:59], v[52:53], v[58:59]
	v_pk_mul_f32 v[60:61], v[54:55], v[60:61]
	v_pk_mul_f32 v[64:65], v[50:51], v[64:65]
	v_pk_mul_f32 v[62:63], v[48:49], v[62:63]
	s_mov_b64 s[0:1], 0

;     __device__ __forceinline__ void operator()(const f32x4 (&acc)[2][2][4][2], const Unit& u, int wr, int wc, int fr, int fq) const {
;     ...
;                     const int c0 = u.pn * BM + bj * HALF + wc * 32 + 8 * fq;
;                     f32x4 v0 = acc[ai][bj][m][0] * rs, v1 = acc[ai][bj][m][1] * rs;
;                     if (kind <= 1) {
;                         float s = (v0[0] * v0[0] + v0[1] * v0[1]) + (v0[2] * v0[2] + v0[3] * v0[3]) + (v1[0] * v1[0] + v1[1] * v1[1]) + (v1[2] * v1[2] + v1[3] * v1[3]);
;                         s += __shfl_xor(s, 16); s += __shfl_xor(s, 32);
;                         const int head = (u.pn & 3) * 2 + bj;
;                         if (fq == 0) ssq[(size_t)((kind * 8 + head) * 4 + wc) * MT + row] = s;
;                     } else if (kind <= 3) {
;                         const int i0 = (c0 & 127) >> 1;
;                         const f32x4 csa = *(const f32x4*)(cs + (size_t)pos * 64 + i0), csb = *(const f32x4*)(cs + (size_t)pos * 64 + i0 + 2);
;                         const float sc = (kind == 3) ? KSCALE : 1.0f;
;                         f32x4 w0, w1;
;                         w0[0] = (v0[0] * csa[0] - v0[1] * csa[1]) * sc; w0[1] = (v0[1] * csa[0] + v0[0] * csa[1]) * sc;
;                         w0[2] = (v0[2] * csa[2] - v0[3] * csa[3]) * sc; w0[3] = (v0[3] * csa[2] + v0[2] * csa[3]) * sc;
;                         w1[0] = (v1[0] * csb[0] - v1[1] * csb[1]) * sc; w1[1] = (v1[1] * csb[0] + v1[0] * csb[1]) * sc;
;                         w1[2] = (v1[2] * csb[2] - v1[3] * csb[3]) * sc; w1[3] = (v1[3] * csb[2] + v1[2] * csb[3]) * sc;
;                         v0 = w0; v1 = w1;
;                     } else {
; #pragma unroll
;                         for (int j = 0; j < 4; ++j) { v0[j] = v0[j] * __builtin_amdgcn_rcpf(1.0f + __builtin_amdgcn_exp2f(-1.4426950408889634f * v0[j]));
;                                                       v1[j] = v1[j] * __builtin_amdgcn_rcpf(1.0f + __builtin_amdgcn_exp2f(-1.4426950408889634f * v1[j])); }
;                     }
;                     u32x4 w; w.x = cvt_pk_bf16(v0[0], v0[1]); w.y = cvt_pk_bf16(v0[2], v0[3]); w.z = cvt_pk_bf16(v1[0], v1[1]); w.w = cvt_pk_bf16(v1[2], v1[3]);
;                     *(u32x4*)(O + (size_t)row * TOKP + c0) = w;
.LBB0_336:
	v_mov_b64_e32 v[40:41], s[80:81]
	s_movk_i32 s0, 0x2900
	v_mad_i64_i32 v[40:41], s[0:1], v59, s0, v[40:41]
	v_cvt_pk_bf16_f32 v42, v50, v51
	v_cvt_pk_bf16_f32 v43, v52, v53
	v_lshl_add_u64 v[40:41], v[120:121], 1, v[40:41]
	v_mov_b32_e32 v49, v48
	v_cvt_pk_bf16_f32 v44, v54, v55
	v_cvt_pk_bf16_f32 v45, v56, v57
	v_and_b32_e32 v244, -16, v59
	v_lshlrev_b32_e32 v244, v233, v244
	v_mov_b32_e32 v245, 0
	v_lshl_add_u64 v[246:247], v[244:245], 0, v[238:239]
	v_cndmask_b32_e64 v246, v40, v246, s[100:101]
	v_cndmask_b32_e64 v247, v41, v247, s[100:101]
	v_lshl_add_u64 v[248:249], v[246:247], 0, v[242:243]
	global_store_dwordx4 v[246:247], v[42:45], off
	v_pk_mul_f32 v[36:37], v[36:37], v[48:49]
	v_pk_mul_f32 v[32:33], v[32:33], v[48:49]
	v_mov_b32_e32 v42, v48
	v_mov_b32_e32 v43, v48
	v_pk_mul_f32 v[38:39], v[38:39], v[42:43]
	v_pk_mul_f32 v[34:35], v[34:35], v[42:43]
	s_and_b64 vcc, exec, s[40:41]
	s_mov_b64 s[0:1], -1
	s_cbranch_vccnz .LBB0_342
	s_and_b64 vcc, exec, s[38:39]
	s_cbranch_vccnz .LBB0_339
	v_mul_f32_e32 v43, 0xbfb8aa3b, v32
	v_mul_f32_e32 v44, 0xbfb8aa3b, v37
	v_exp_f32_e32 v43, v43
	v_exp_f32_e32 v44, v44
	v_mul_f32_e32 v45, 0xbfb8aa3b, v38
	v_mul_f32_e32 v47, 0xbfb8aa3b, v34
	v_add_f32_e32 v43, 1.0, v43
	v_rcp_f32_e32 v46, v43
	v_add_f32_e32 v43, 1.0, v44
	v_mul_f32_e32 v44, 0xbfb8aa3b, v33
	v_exp_f32_e32 v44, v44
	v_exp_f32_e32 v45, v45
	v_exp_f32_e32 v47, v47
	v_mul_f32_e32 v42, 0xbfb8aa3b, v36
	v_add_f32_e32 v50, 1.0, v44
	v_add_f32_e32 v44, 1.0, v45
	v_add_f32_e32 v45, 1.0, v47
	v_mul_f32_e32 v47, 0xbfb8aa3b, v39
	v_mul_f32_e32 v48, 0xbfb8aa3b, v35
	v_exp_f32_e32 v42, v42
	v_exp_f32_e32 v47, v47
	v_exp_f32_e32 v49, v48
	v_rcp_f32_e32 v48, v45
	v_add_f32_e32 v42, 1.0, v42
	v_add_f32_e32 v45, 1.0, v47
	v_add_f32_e32 v47, 1.0, v49
	v_rcp_f32_e32 v42, v42
	v_rcp_f32_e32 v43, v43
	v_rcp_f32_e32 v44, v44
	v_rcp_f32_e32 v45, v45
	v_rcp_f32_e32 v49, v47
	v_rcp_f32_e32 v47, v50
	v_pk_mul_f32 v[42:43], v[36:37], v[42:43]
	v_pk_mul_f32 v[44:45], v[38:39], v[44:45]
	v_pk_mul_f32 v[48:49], v[34:35], v[48:49]
	v_pk_mul_f32 v[46:47], v[32:33], v[46:47]
	s_mov_b64 s[0:1], 0

;     __device__ __forceinline__ void operator()(const f32x4 (&acc)[2][2][4][2], const Unit& u, int wr, int wc, int fr, int fq) const {
;     ...
;                     const int c0 = u.pn * BM + bj * HALF + wc * 32 + 8 * fq;
;                     f32x4 v0 = acc[ai][bj][m][0] * rs, v1 = acc[ai][bj][m][1] * rs;
;                     if (kind <= 1) {
;                         float s = (v0[0] * v0[0] + v0[1] * v0[1]) + (v0[2] * v0[2] + v0[3] * v0[3]) + (v1[0] * v1[0] + v1[1] * v1[1]) + (v1[2] * v1[2] + v1[3] * v1[3]);
;                         s += __shfl_xor(s, 16); s += __shfl_xor(s, 32);
;                         const int head = (u.pn & 3) * 2 + bj;
;                         if (fq == 0) ssq[(size_t)((kind * 8 + head) * 4 + wc) * MT + row] = s;
;                     } else if (kind <= 3) {
;                         const int i0 = (c0 & 127) >> 1;
;                         const f32x4 csa = *(const f32x4*)(cs + (size_t)pos * 64 + i0), csb = *(const f32x4*)(cs + (size_t)pos * 64 + i0 + 2);
;                         const float sc = (kind == 3) ? KSCALE : 1.0f;
;                         f32x4 w0, w1;
;                         w0[0] = (v0[0] * csa[0] - v0[1] * csa[1]) * sc; w0[1] = (v0[1] * csa[0] + v0[0] * csa[1]) * sc;
;                         w0[2] = (v0[2] * csa[2] - v0[3] * csa[3]) * sc; w0[3] = (v0[3] * csa[2] + v0[2] * csa[3]) * sc;
;                         w1[0] = (v1[0] * csb[0] - v1[1] * csb[1]) * sc; w1[1] = (v1[1] * csb[0] + v1[0] * csb[1]) * sc;
;                         w1[2] = (v1[2] * csb[2] - v1[3] * csb[3]) * sc; w1[3] = (v1[3] * csb[2] + v1[2] * csb[3]) * sc;
;                         v0 = w0; v1 = w1;
;                     } else {
; #pragma unroll
;                         for (int j = 0; j < 4; ++j) { v0[j] = v0[j] * __builtin_amdgcn_rcpf(1.0f + __builtin_amdgcn_exp2f(-1.4426950408889634f * v0[j]));
;                                                       v1[j] = v1[j] * __builtin_amdgcn_rcpf(1.0f + __builtin_amdgcn_exp2f(-1.4426950408889634f * v1[j])); }
;                     }
;                     u32x4 w; w.x = cvt_pk_bf16(v0[0], v0[1]); w.y = cvt_pk_bf16(v0[2], v0[3]); w.z = cvt_pk_bf16(v1[0], v1[1]); w.w = cvt_pk_bf16(v1[2], v1[3]);
;                     *(u32x4*)(O + (size_t)row * TOKP + c0) = w;
.LBB0_356:
	v_mov_b64_e32 v[24:25], s[80:81]
	s_movk_i32 s0, 0x2900
	v_mad_i64_i32 v[24:25], s[0:1], v43, s0, v[24:25]
	v_cvt_pk_bf16_f32 v26, v34, v35
	v_cvt_pk_bf16_f32 v27, v36, v37
	v_lshl_add_u64 v[24:25], v[120:121], 1, v[24:25]
	v_mov_b32_e32 v33, v32
	v_cvt_pk_bf16_f32 v28, v38, v39
	v_cvt_pk_bf16_f32 v29, v40, v41
	v_and_b32_e32 v244, -16, v43
	v_lshlrev_b32_e32 v244, v233, v244
	v_mov_b32_e32 v245, 0
	v_lshl_add_u64 v[246:247], v[244:245], 0, v[238:239]
	v_cndmask_b32_e64 v246, v24, v246, s[100:101]
	v_cndmask_b32_e64 v247, v25, v247, s[100:101]
	v_lshl_add_u64 v[248:249], v[246:247], 0, v[242:243]
	global_store_dwordx4 v[246:247], v[26:29], off
	v_pk_mul_f32 v[20:21], v[20:21], v[32:33]
	v_pk_mul_f32 v[16:17], v[16:17], v[32:33]
	v_mov_b32_e32 v26, v32
	v_mov_b32_e32 v27, v32
	v_pk_mul_f32 v[22:23], v[22:23], v[26:27]
	v_pk_mul_f32 v[18:19], v[18:19], v[26:27]
	s_and_b64 vcc, exec, s[40:41]
	s_mov_b64 s[0:1], -1
	s_cbranch_vccnz .LBB0_362
	s_and_b64 vcc, exec, s[38:39]
	s_cbranch_vccnz .LBB0_359
	v_mul_f32_e32 v27, 0xbfb8aa3b, v16
	v_mul_f32_e32 v28, 0xbfb8aa3b, v21
	v_exp_f32_e32 v27, v27
	v_exp_f32_e32 v28, v28
	v_mul_f32_e32 v29, 0xbfb8aa3b, v22
	v_mul_f32_e32 v31, 0xbfb8aa3b, v18
	v_add_f32_e32 v27, 1.0, v27
	v_rcp_f32_e32 v30, v27
	v_add_f32_e32 v27, 1.0, v28
	v_mul_f32_e32 v28, 0xbfb8aa3b, v17
	v_exp_f32_e32 v28, v28
	v_exp_f32_e32 v29, v29
	v_exp_f32_e32 v31, v31
	v_mul_f32_e32 v26, 0xbfb8aa3b, v20
	v_add_f32_e32 v34, 1.0, v28
	v_add_f32_e32 v28, 1.0, v29
	v_add_f32_e32 v29, 1.0, v31
	v_mul_f32_e32 v31, 0xbfb8aa3b, v23
	v_mul_f32_e32 v32, 0xbfb8aa3b, v19
	v_exp_f32_e32 v26, v26
	v_exp_f32_e32 v31, v31
	v_exp_f32_e32 v33, v32
	v_rcp_f32_e32 v32, v29
	v_add_f32_e32 v26, 1.0, v26
	v_add_f32_e32 v29, 1.0, v31
	v_add_f32_e32 v31, 1.0, v33
	v_rcp_f32_e32 v26, v26
	v_rcp_f32_e32 v27, v27
	v_rcp_f32_e32 v28, v28
	v_rcp_f32_e32 v29, v29
	v_rcp_f32_e32 v33, v31
	v_rcp_f32_e32 v31, v34
	v_pk_mul_f32 v[26:27], v[20:21], v[26:27]
	v_pk_mul_f32 v[28:29], v[22:23], v[28:29]
	v_pk_mul_f32 v[32:33], v[18:19], v[32:33]
	v_pk_mul_f32 v[30:31], v[16:17], v[30:31]
	s_mov_b64 s[0:1], 0

;     __device__ __forceinline__ void operator()(const f32x4 (&acc)[2][2][4][2], const Unit& u, int wr, int wc, int fr, int fq) const {
;     ...
;                     const int c0 = u.pn * BM + bj * HALF + wc * 32 + 8 * fq;
;                     f32x4 v0 = acc[ai][bj][m][0] * rs, v1 = acc[ai][bj][m][1] * rs;
;                     if (kind <= 1) {
;                         float s = (v0[0] * v0[0] + v0[1] * v0[1]) + (v0[2] * v0[2] + v0[3] * v0[3]) + (v1[0] * v1[0] + v1[1] * v1[1]) + (v1[2] * v1[2] + v1[3] * v1[3]);
;                         s += __shfl_xor(s, 16); s += __shfl_xor(s, 32);
;                         const int head = (u.pn & 3) * 2 + bj;
;                         if (fq == 0) ssq[(size_t)((kind * 8 + head) * 4 + wc) * MT + row] = s;
;                     } else if (kind <= 3) {
;                         const int i0 = (c0 & 127) >> 1;
;                         const f32x4 csa = *(const f32x4*)(cs + (size_t)pos * 64 + i0), csb = *(const f32x4*)(cs + (size_t)pos * 64 + i0 + 2);
;                         const float sc = (kind == 3) ? KSCALE : 1.0f;
;                         f32x4 w0, w1;
;                         w0[0] = (v0[0] * csa[0] - v0[1] * csa[1]) * sc; w0[1] = (v0[1] * csa[0] + v0[0] * csa[1]) * sc;
;                         w0[2] = (v0[2] * csa[2] - v0[3] * csa[3]) * sc; w0[3] = (v0[3] * csa[2] + v0[2] * csa[3]) * sc;
;                         w1[0] = (v1[0] * csb[0] - v1[1] * csb[1]) * sc; w1[1] = (v1[1] * csb[0] + v1[0] * csb[1]) * sc;
;                         w1[2] = (v1[2] * csb[2] - v1[3] * csb[3]) * sc; w1[3] = (v1[3] * csb[2] + v1[2] * csb[3]) * sc;
;                         v0 = w0; v1 = w1;
;                     } else {
; #pragma unroll
;                         for (int j = 0; j < 4; ++j) { v0[j] = v0[j] * __builtin_amdgcn_rcpf(1.0f + __builtin_amdgcn_exp2f(-1.4426950408889634f * v0[j]));
;                                                       v1[j] = v1[j] * __builtin_amdgcn_rcpf(1.0f + __builtin_amdgcn_exp2f(-1.4426950408889634f * v1[j])); }
;                     }
;                     u32x4 w; w.x = cvt_pk_bf16(v0[0], v0[1]); w.y = cvt_pk_bf16(v0[2], v0[3]); w.z = cvt_pk_bf16(v1[0], v1[1]); w.w = cvt_pk_bf16(v1[2], v1[3]);
;                     *(u32x4*)(O + (size_t)row * TOKP + c0) = w;
.LBB0_376:
	v_mov_b64_e32 v[8:9], s[80:81]
	s_movk_i32 s0, 0x2900
	v_mad_i64_i32 v[8:9], s[0:1], v27, s0, v[8:9]
	v_cvt_pk_bf16_f32 v10, v18, v19
	v_cvt_pk_bf16_f32 v11, v20, v21
	v_lshl_add_u64 v[8:9], v[120:121], 1, v[8:9]
	v_mov_b32_e32 v17, v16
	v_cvt_pk_bf16_f32 v12, v22, v23
	v_cvt_pk_bf16_f32 v13, v24, v25
	v_and_b32_e32 v244, -16, v27
	v_lshlrev_b32_e32 v244, v233, v244
	v_mov_b32_e32 v245, 0
	v_lshl_add_u64 v[246:247], v[244:245], 0, v[238:239]
	v_cndmask_b32_e64 v246, v8, v246, s[100:101]
	v_cndmask_b32_e64 v247, v9, v247, s[100:101]
	v_lshl_add_u64 v[248:249], v[246:247], 0, v[242:243]
	global_store_dwordx4 v[246:247], v[10:13], off
	s_and_b64 vcc, exec, s[40:41]
	v_readlane_b32 s40, v250, 32
	v_mov_b32_e32 v10, v16
	v_mov_b32_e32 v11, v16
	v_pk_mul_f32 v[6:7], v[6:7], v[10:11]
	v_pk_mul_f32 v[4:5], v[4:5], v[16:17]
	v_pk_mul_f32 v[2:3], v[2:3], v[10:11]
	v_pk_mul_f32 v[0:1], v[0:1], v[16:17]
	s_mov_b64 s[0:1], -1
	v_readlane_b32 s41, v250, 33
	s_cbranch_vccnz .LBB0_382
	s_and_b64 vcc, exec, s[38:39]
	s_cbranch_vccnz .LBB0_379
	v_mul_f32_e32 v11, 0xbfb8aa3b, v0
	v_mul_f32_e32 v12, 0xbfb8aa3b, v5
	v_exp_f32_e32 v11, v11
	v_exp_f32_e32 v12, v12
	v_mul_f32_e32 v13, 0xbfb8aa3b, v6
	v_mul_f32_e32 v15, 0xbfb8aa3b, v2
	v_add_f32_e32 v11, 1.0, v11
	v_rcp_f32_e32 v14, v11
	v_add_f32_e32 v11, 1.0, v12
	v_mul_f32_e32 v12, 0xbfb8aa3b, v1
	v_exp_f32_e32 v12, v12
	v_exp_f32_e32 v13, v13
	v_exp_f32_e32 v15, v15
	v_mul_f32_e32 v10, 0xbfb8aa3b, v4
	v_add_f32_e32 v18, 1.0, v12
	v_add_f32_e32 v12, 1.0, v13
	v_add_f32_e32 v13, 1.0, v15
	v_mul_f32_e32 v15, 0xbfb8aa3b, v7
	v_mul_f32_e32 v16, 0xbfb8aa3b, v3
	v_exp_f32_e32 v10, v10
	v_exp_f32_e32 v15, v15
	v_exp_f32_e32 v17, v16
	v_rcp_f32_e32 v16, v13
	v_add_f32_e32 v10, 1.0, v10
	v_add_f32_e32 v13, 1.0, v15
	v_add_f32_e32 v15, 1.0, v17
	v_rcp_f32_e32 v10, v10
	v_rcp_f32_e32 v11, v11
	v_rcp_f32_e32 v12, v12
	v_rcp_f32_e32 v13, v13
	v_rcp_f32_e32 v17, v15
	v_rcp_f32_e32 v15, v18
	v_pk_mul_f32 v[10:11], v[4:5], v[10:11]
	v_pk_mul_f32 v[12:13], v[6:7], v[12:13]
	v_pk_mul_f32 v[16:17], v[2:3], v[16:17]
	v_pk_mul_f32 v[14:15], v[0:1], v[14:15]
	s_mov_b64 s[0:1], 0

; __device__ __forceinline__ unsigned cvt_pk_bf16(float lo, float hi) { unsigned r; asm volatile("v_cvt_pk_bf16_f32 %0, %1, %2" : "=v"(r) : "v"(lo), "v"(hi)); return r; }
;     __device__ __forceinline__ void operator()(const f32x4 (&acc)[2][2][4][2], const Unit& u, int wr, int wc, int fr, int fq) const {
;         const int row0 = u.pm * BM + wr * 64 + fr, col0 = u.pn * BM + wc * 32 + 8 * fq;
;         f32x4 ra[2], rb[2];
; #pragma unroll
;         for (int bj = 0; bj < 2; ++bj) { ra[bj] = *(const f32x4*)(rstd + col0 + bj * HALF); rb[bj] = *(const f32x4*)(rstd + col0 + bj * HALF + 4); }
; #pragma unroll
;         for (int ai = 0; ai < 2; ++ai)
; #pragma unroll
;             for (int m = 0; m < 4; ++m) { bf16_t* rowp = O + (size_t)(row0 + ai * HALF + m * 16) * ldc + col0;
; #pragma unroll
;                 for (int bj = 0; bj < 2; ++bj) { const f32x4 v0 = acc[ai][bj][m][0] * ra[bj], v1 = acc[ai][bj][m][1] * rb[bj];
;                     u32x4 w; w.x = cvt_pk_bf16(v0[0], v0[1]); w.y = cvt_pk_bf16(v0[2], v0[3]); w.z = cvt_pk_bf16(v1[0], v1[1]); w.w = cvt_pk_bf16(v1[2], v1[3]);
;                     *(u32x4*)(rowp + bj * HALF) = w; } }
.LBB0_406:
	s_cmp_gt_u32 s40, 3
	s_cselect_b32 s100, -1, 0
	s_mov_b32 s101, s100
	v_mov_b32_e32 v226, s41
	v_lshlrev_b32_e32 v226, 13, v226
	v_lshl_add_u32 v226, v160, 5, v226
	v_and_b32_e32 v227, 15, v158
	v_lshl_add_u32 v226, v227, 4, v226
	v_add_u32_e32 v226, 0x2ec00000, v226
	v_mov_b32_e32 v227, 0
	v_mov_b32_e32 v228, s62
	v_mov_b32_e32 v229, s63
	v_lshl_add_u64 v[228:229], v[228:229], 0, v[226:227]
	v_mov_b32_e32 v230, 0x100
	v_mov_b32_e32 v232, 0x1000
	v_cndmask_b32_e64 v230, v230, v232, s[100:101]
	v_mov_b32_e32 v231, 0
	v_lshl_or_b32 v156, s41, 8, v160
	v_ashrrev_i32_e32 v157, 31, v156
	v_lshl_add_u64 v[100:101], v[156:157], 2, s[56:57]
	global_load_dwordx4 v[104:107], v[100:101], off offset:16
	global_load_dwordx4 v[112:115], v[100:101], off
	global_load_dwordx4 v[96:99], v[100:101], off offset:528
	s_nop 0
	global_load_dwordx4 v[100:103], v[100:101], off offset:512
	v_lshl_add_u32 v162, s40, 8, v158
	v_mov_b64_e32 v[154:155], s[64:65]
	s_mov_b32 s4, 0x8100
	v_and_b32_e32 v232, -16, v162
	v_lshlrev_b32_e32 v232, 15, v232
	v_mad_i64_i32 v[164:165], s[2:3], v162, s4, v[154:155]
	v_lshlrev_b64 v[156:157], 1, v[156:157]
	v_lshl_add_u64 v[164:165], v[164:165], 0, v[156:157]
	s_andn2_b64 vcc, exec, s[34:35]
	s_mov_b64 s[22:23], 0x800
	s_waitcnt vmcnt(0)
	v_pk_mul_f32 v[166:167], v[138:139], v[106:107]
	v_pk_mul_f32 v[142:143], v[142:143], v[114:115]
	v_pk_mul_f32 v[140:141], v[140:141], v[112:113]
	v_pk_mul_f32 v[138:139], v[136:137], v[104:105]
	v_cvt_pk_bf16_f32 v136, v140, v141
	v_cvt_pk_bf16_f32 v137, v142, v143
	v_pk_mul_f32 v[132:133], v[132:133], v[100:101]
	v_cvt_pk_bf16_f32 v138, v138, v139
	v_cvt_pk_bf16_f32 v139, v166, v167
	v_mov_b32_e32 v233, 0
	v_lshl_add_u64 v[234:235], v[232:233], 0, v[228:229]
	v_cndmask_b32_e64 v234, v164, v234, s[100:101]
	v_cndmask_b32_e64 v235, v165, v235, s[100:101]
	v_lshl_add_u64 v[236:237], v[234:235], 0, v[230:231]
	global_store_dwordx4 v[234:235], v[136:139], off
	v_pk_mul_f32 v[134:135], v[134:135], v[102:103]
	v_pk_mul_f32 v[126:127], v[126:127], v[114:115]
	v_pk_mul_f32 v[136:137], v[130:131], v[98:99]
	v_pk_mul_f32 v[130:131], v[128:129], v[96:97]
	v_cvt_pk_bf16_f32 v128, v132, v133
	v_cvt_pk_bf16_f32 v129, v134, v135
	v_pk_mul_f32 v[124:125], v[124:125], v[112:113]
	v_cvt_pk_bf16_f32 v130, v130, v131
	v_cvt_pk_bf16_f32 v131, v136, v137
	global_store_dwordx4 v[236:237], v[128:131], off
	v_pk_mul_f32 v[116:117], v[116:117], v[100:101]
	v_pk_mul_f32 v[118:119], v[118:119], v[102:103]
	v_or_b32_e32 v128, 16, v162
	v_and_b32_e32 v232, -16, v128
	v_lshlrev_b32_e32 v232, 15, v232
	v_mad_i64_i32 v[128:129], s[2:3], v128, s4, v[154:155]
	v_lshl_add_u64 v[128:129], v[128:129], 0, v[156:157]
	v_pk_mul_f32 v[130:131], v[122:123], v[106:107]
	v_pk_mul_f32 v[122:123], v[120:121], v[104:105]
	v_cvt_pk_bf16_f32 v120, v124, v125
	v_cvt_pk_bf16_f32 v121, v126, v127
	v_pk_mul_f32 v[94:95], v[94:95], v[114:115]
	v_cvt_pk_bf16_f32 v122, v122, v123
	v_cvt_pk_bf16_f32 v123, v130, v131
	v_mov_b32_e32 v233, 0
	v_lshl_add_u64 v[234:235], v[232:233], 0, v[228:229]
	v_cndmask_b32_e64 v234, v128, v234, s[100:101]
	v_cndmask_b32_e64 v235, v129, v235, s[100:101]
	v_lshl_add_u64 v[236:237], v[234:235], 0, v[230:231]
	global_store_dwordx4 v[234:235], v[120:123], off
	v_pk_mul_f32 v[92:93], v[92:93], v[112:113]
	v_pk_mul_f32 v[84:85], v[84:85], v[100:101]
	v_pk_mul_f32 v[120:121], v[110:111], v[98:99]
	v_pk_mul_f32 v[110:111], v[108:109], v[96:97]
	v_cvt_pk_bf16_f32 v108, v116, v117
	v_cvt_pk_bf16_f32 v109, v118, v119
	v_pk_mul_f32 v[86:87], v[86:87], v[102:103]
	v_cvt_pk_bf16_f32 v110, v110, v111
	v_cvt_pk_bf16_f32 v111, v120, v121
	global_store_dwordx4 v[236:237], v[108:111], off
	v_pk_mul_f32 v[78:79], v[78:79], v[114:115]
	v_pk_mul_f32 v[76:77], v[76:77], v[112:113]
	v_or_b32_e32 v108, 32, v162
	v_and_b32_e32 v232, -16, v108
	v_lshlrev_b32_e32 v232, 15, v232
	v_mad_i64_i32 v[108:109], s[2:3], v108, s4, v[154:155]
	v_lshl_add_u64 v[108:109], v[108:109], 0, v[156:157]
	v_pk_mul_f32 v[110:111], v[90:91], v[106:107]
	v_pk_mul_f32 v[90:91], v[88:89], v[104:105]
	v_cvt_pk_bf16_f32 v88, v92, v93
	v_cvt_pk_bf16_f32 v89, v94, v95
	v_pk_mul_f32 v[68:69], v[68:69], v[100:101]
	v_cvt_pk_bf16_f32 v90, v90, v91
	v_cvt_pk_bf16_f32 v91, v110, v111
	v_mov_b32_e32 v233, 0
	v_lshl_add_u64 v[234:235], v[232:233], 0, v[228:229]
	v_cndmask_b32_e64 v234, v108, v234, s[100:101]
	v_cndmask_b32_e64 v235, v109, v235, s[100:101]
	v_lshl_add_u64 v[236:237], v[234:235], 0, v[230:231]
	global_store_dwordx4 v[234:235], v[88:91], off
	v_pk_mul_f32 v[70:71], v[70:71], v[102:103]
	v_pk_mul_f32 v[62:63], v[62:63], v[114:115]
	v_pk_mul_f32 v[88:89], v[82:83], v[98:99]
	v_pk_mul_f32 v[82:83], v[80:81], v[96:97]
	v_cvt_pk_bf16_f32 v80, v84, v85
	v_cvt_pk_bf16_f32 v81, v86, v87
	v_pk_mul_f32 v[60:61], v[60:61], v[112:113]
	v_cvt_pk_bf16_f32 v82, v82, v83
	v_cvt_pk_bf16_f32 v83, v88, v89
	global_store_dwordx4 v[236:237], v[80:83], off
	v_pk_mul_f32 v[52:53], v[52:53], v[100:101]
	v_pk_mul_f32 v[54:55], v[54:55], v[102:103]
	v_or_b32_e32 v80, 48, v162
	v_and_b32_e32 v232, -16, v80
	v_lshlrev_b32_e32 v232, 15, v232
	v_mad_i64_i32 v[80:81], s[2:3], v80, s4, v[154:155]
	v_lshl_add_u64 v[80:81], v[80:81], 0, v[156:157]
	v_pk_mul_f32 v[82:83], v[74:75], v[106:107]
	v_pk_mul_f32 v[74:75], v[72:73], v[104:105]
; __device__ __forceinline__ unsigned cvt_pk_bf16(float lo, float hi) { unsigned r; asm volatile("v_cvt_pk_bf16_f32 %0, %1, %2" : "=v"(r) : "v"(lo), "v"(hi)); return r; }
;     __device__ __forceinline__ void operator()(const f32x4 (&acc)[2][2][4][2], const Unit& u, int wr, int wc, int fr, int fq) const {
;     ...
;         for (int ai = 0; ai < 2; ++ai)
; #pragma unroll
;             for (int m = 0; m < 4; ++m) { bf16_t* rowp = O + (size_t)(row0 + ai * HALF + m * 16) * ldc + col0;
; #pragma unroll
;                 for (int bj = 0; bj < 2; ++bj) { const f32x4 v0 = acc[ai][bj][m][0] * ra[bj], v1 = acc[ai][bj][m][1] * rb[bj];
;                     u32x4 w; w.x = cvt_pk_bf16(v0[0], v0[1]); w.y = cvt_pk_bf16(v0[2], v0[3]); w.z = cvt_pk_bf16(v1[0], v1[1]); w.w = cvt_pk_bf16(v1[2], v1[3]);
;                     *(u32x4*)(rowp + bj * HALF) = w; } }
	v_cvt_pk_bf16_f32 v72, v76, v77
	v_cvt_pk_bf16_f32 v73, v78, v79
	v_pk_mul_f32 v[48:49], v[48:49], v[112:113]
	v_cvt_pk_bf16_f32 v74, v74, v75
	v_cvt_pk_bf16_f32 v75, v82, v83
	v_mov_b32_e32 v233, 0
	v_lshl_add_u64 v[234:235], v[232:233], 0, v[228:229]
	v_cndmask_b32_e64 v234, v80, v234, s[100:101]
	v_cndmask_b32_e64 v235, v81, v235, s[100:101]
	v_lshl_add_u64 v[236:237], v[234:235], 0, v[230:231]
	global_store_dwordx4 v[234:235], v[72:75], off
	v_pk_mul_f32 v[36:37], v[36:37], v[100:101]
	v_pk_mul_f32 v[38:39], v[38:39], v[102:103]
	v_pk_mul_f32 v[72:73], v[66:67], v[98:99]
	v_pk_mul_f32 v[66:67], v[64:65], v[96:97]
	v_cvt_pk_bf16_f32 v64, v68, v69
	v_cvt_pk_bf16_f32 v65, v70, v71
	v_pk_mul_f32 v[32:33], v[32:33], v[112:113]
	v_cvt_pk_bf16_f32 v66, v66, v67
	v_cvt_pk_bf16_f32 v67, v72, v73
	global_store_dwordx4 v[236:237], v[64:67], off
	v_pk_mul_f32 v[20:21], v[20:21], v[100:101]
	v_pk_mul_f32 v[22:23], v[22:23], v[102:103]
	v_add_u32_e32 v64, 0x80, v162
	v_and_b32_e32 v232, -16, v64
	v_lshlrev_b32_e32 v232, 15, v232
	v_mad_i64_i32 v[64:65], s[2:3], v64, s4, v[154:155]
	v_lshl_add_u64 v[64:65], v[64:65], 0, v[156:157]
	v_pk_mul_f32 v[66:67], v[58:59], v[106:107]
	v_pk_mul_f32 v[58:59], v[56:57], v[104:105]
	v_cvt_pk_bf16_f32 v56, v60, v61
	v_cvt_pk_bf16_f32 v57, v62, v63
	v_pk_mul_f32 v[16:17], v[16:17], v[112:113]
	v_cvt_pk_bf16_f32 v58, v58, v59
	v_cvt_pk_bf16_f32 v59, v66, v67
	v_mov_b32_e32 v233, 0
	v_lshl_add_u64 v[234:235], v[232:233], 0, v[228:229]
	v_cndmask_b32_e64 v234, v64, v234, s[100:101]
	v_cndmask_b32_e64 v235, v65, v235, s[100:101]
	v_lshl_add_u64 v[236:237], v[234:235], 0, v[230:231]
	global_store_dwordx4 v[234:235], v[56:59], off
	v_pk_mul_f32 v[6:7], v[6:7], v[102:103]
	v_pk_mul_f32 v[4:5], v[4:5], v[100:101]
	v_pk_mul_f32 v[56:57], v[46:47], v[98:99]
	v_pk_mul_f32 v[46:47], v[44:45], v[96:97]
	v_cvt_pk_bf16_f32 v44, v52, v53
	v_cvt_pk_bf16_f32 v45, v54, v55
	s_nop 0
	v_cvt_pk_bf16_f32 v46, v46, v47
	v_cvt_pk_bf16_f32 v47, v56, v57
	global_store_dwordx4 v[236:237], v[44:47], off
	s_nop 1
	v_add_u32_e32 v44, 0x90, v162
	v_and_b32_e32 v232, -16, v44
	v_lshlrev_b32_e32 v232, 15, v232
	v_mad_i64_i32 v[44:45], s[2:3], v44, s4, v[154:155]
	v_lshl_add_u64 v[44:45], v[44:45], 0, v[156:157]
	v_pk_mul_f32 v[46:47], v[50:51], v[114:115]
	v_pk_mul_f32 v[50:51], v[42:43], v[106:107]
	v_pk_mul_f32 v[42:43], v[40:41], v[104:105]
	v_cvt_pk_bf16_f32 v40, v48, v49
	v_cvt_pk_bf16_f32 v41, v46, v47
	s_nop 0
	v_cvt_pk_bf16_f32 v42, v42, v43
	v_cvt_pk_bf16_f32 v43, v50, v51
	v_mov_b32_e32 v233, 0
	v_lshl_add_u64 v[234:235], v[232:233], 0, v[228:229]
	v_cndmask_b32_e64 v234, v44, v234, s[100:101]
	v_cndmask_b32_e64 v235, v45, v235, s[100:101]
	v_lshl_add_u64 v[236:237], v[234:235], 0, v[230:231]
	global_store_dwordx4 v[234:235], v[40:43], off
	s_nop 1
	v_pk_mul_f32 v[40:41], v[30:31], v[98:99]
	v_pk_mul_f32 v[30:31], v[28:29], v[96:97]
	v_cvt_pk_bf16_f32 v28, v36, v37
	v_cvt_pk_bf16_f32 v29, v38, v39
	s_nop 0
	v_cvt_pk_bf16_f32 v30, v30, v31
	v_cvt_pk_bf16_f32 v31, v40, v41
	global_store_dwordx4 v[236:237], v[28:31], off
	s_nop 1
	v_add_u32_e32 v28, 0xa0, v162
	v_and_b32_e32 v232, -16, v28
	v_lshlrev_b32_e32 v232, 15, v232
	v_mad_i64_i32 v[28:29], s[2:3], v28, s4, v[154:155]
	v_lshl_add_u64 v[28:29], v[28:29], 0, v[156:157]
	v_pk_mul_f32 v[30:31], v[34:35], v[114:115]
	v_pk_mul_f32 v[34:35], v[26:27], v[106:107]
	v_pk_mul_f32 v[26:27], v[24:25], v[104:105]
	v_cvt_pk_bf16_f32 v24, v32, v33
	v_cvt_pk_bf16_f32 v25, v30, v31
	s_nop 0
	v_cvt_pk_bf16_f32 v26, v26, v27
	v_cvt_pk_bf16_f32 v27, v34, v35
	v_mov_b32_e32 v233, 0
	v_lshl_add_u64 v[234:235], v[232:233], 0, v[228:229]
	v_cndmask_b32_e64 v234, v28, v234, s[100:101]
	v_cndmask_b32_e64 v235, v29, v235, s[100:101]
	v_lshl_add_u64 v[236:237], v[234:235], 0, v[230:231]
	global_store_dwordx4 v[234:235], v[24:27], off
	s_nop 1
	v_pk_mul_f32 v[24:25], v[14:15], v[98:99]
	v_pk_mul_f32 v[14:15], v[12:13], v[96:97]
	v_cvt_pk_bf16_f32 v12, v20, v21
	v_cvt_pk_bf16_f32 v13, v22, v23
	s_nop 0
	v_cvt_pk_bf16_f32 v14, v14, v15
	v_cvt_pk_bf16_f32 v15, v24, v25
	global_store_dwordx4 v[236:237], v[12:15], off
	s_nop 1
	v_add_u32_e32 v12, 0xb0, v162
	v_and_b32_e32 v232, -16, v12
	v_lshlrev_b32_e32 v232, 15, v232
	v_mad_i64_i32 v[12:13], s[2:3], v12, s4, v[154:155]
	v_lshl_add_u64 v[12:13], v[12:13], 0, v[156:157]
	v_pk_mul_f32 v[14:15], v[18:19], v[114:115]
	v_pk_mul_f32 v[18:19], v[10:11], v[106:107]
	v_pk_mul_f32 v[10:11], v[8:9], v[104:105]
	v_cvt_pk_bf16_f32 v8, v16, v17
	v_cvt_pk_bf16_f32 v9, v14, v15
	s_mov_b64 s[2:3], -1
	v_cvt_pk_bf16_f32 v10, v10, v11
	v_cvt_pk_bf16_f32 v11, v18, v19
	v_mov_b32_e32 v233, 0
	v_lshl_add_u64 v[234:235], v[232:233], 0, v[228:229]
	v_cndmask_b32_e64 v234, v12, v234, s[100:101]
	v_cndmask_b32_e64 v235, v13, v235, s[100:101]
	v_lshl_add_u64 v[236:237], v[234:235], 0, v[230:231]
	global_store_dwordx4 v[234:235], v[8:11], off
	s_nop 1
	v_pk_mul_f32 v[8:9], v[2:3], v[98:99]
	v_pk_mul_f32 v[2:3], v[0:1], v[96:97]
	v_cvt_pk_bf16_f32 v0, v4, v5
	v_cvt_pk_bf16_f32 v1, v6, v7
	s_nop 0
	v_cvt_pk_bf16_f32 v2, v2, v3
	v_cvt_pk_bf16_f32 v3, v8, v9
	global_store_dwordx4 v[236:237], v[0:3], off
	s_cbranch_vccnz .LBB0_395
	s_andn2_b64 vcc, exec, s[0:1]
	s_cbranch_vccnz .LBB0_394
	s_barrier
	s_branch .LBB0_394

; #define LAS __attribute__((address_space(3)))
; __device__ __forceinline__ int lane_id() { return (int)__builtin_amdgcn_mbcnt_hi(~0u, __builtin_amdgcn_mbcnt_lo(~0u, 0u)); }
; __device__ __forceinline__ float fexp2(float x) { return __builtin_amdgcn_exp2f(x); }
; __device__ __forceinline__ void scan_task(const Frame& F, int task) {
;     int lane = lane_id(); asm volatile("" : "+v"(lane));
;     const int c = lane & 15, rq = lane >> 4;
;     const int eh = task & 1, db = (task >> 1) & 7, h = (task >> 4) & 7, b = task >> 7, bhh = b * NH + h;
;     const bf16* TOK = (const bf16*)(F.ws + WS_TOK); const bf16* SWP = (const bf16*)(F.ws + WS_SWP); bf16* ST = (bf16*)(F.ws + WS_ST);
;     const bf16* kg = TOK + (size_t)(b * S + (lane >> 1)) * TOKP + TK_KR + h * HD + db * 16 + (lane & 1) * 8;
;     const bf16* vrow = SWP + (size_t)(SW_VR + h * HD + eh * 64 + c) * SWPP + b * S + rq * 8;
;     bf16* sp = ST + ((size_t)bhh * NCH * HD + eh * 64 + c) * HD + db * 16 + rq * 4;
;     LAS unsigned char* kt = F.lds + RING_OFF + SC_OFF + F.wave * SC_WAVE_BYTES;
;     LAS unsigned char* kw = kt + (lane >> 1) * SC_PITCH + (lane & 1) * 16;
;     const LAS unsigned char* kr = kt + (rq * 8) * SC_PITCH + c * 2;
;     f32x4 st[4];
; #pragma unroll
;     for (int eb = 0; eb < 4; ++eb) st[eb] = (f32x4){0.f, 0.f, 0.f, 0.f};
;     const float lg = pg8::lg2gamma(h), cd = fexp2(64.f * lg);
;     float dec[16];
; #pragma unroll
;     for (int i = 0; i < 16; ++i) dec[i] = fexp2((float)(63 - ((i >> 3) * 32 + rq * 8 + (i & 7))) * lg);
;     ScanOps o0, o1, o2;
;     scan_load(o0, kg, vrow, 0); scan_load(o1, kg, vrow, 1);
.LBB0_504:
	s_lshr_b32 s0, s8, 4
	s_and_b32 s16, s0, 7
	s_lshl_b32 s0, s2, 1
	s_and_b32 s4, s0, 0xe0
	s_lshl_b32 s0, s16, 8
	v_mov_b32_e32 v184, s0
	s_ashr_i32 s0, s8, 7
	s_lshl_b32 s13, s0, 3
	s_lshl_b32 s0, s0, 11
	v_ashrrev_i32_e32 v6, 1, v0
	v_add_u32_e32 v92, s0, v6
	v_lshrrev_b32_e32 v242, 5, v0
	v_lshlrev_b32_e32 v242, 16, v242
	v_bfe_u32 v243, v0, 1, 4
	v_lshl_add_u32 v242, v243, 4, v242
	v_and_b32_e32 v243, 1, v0
	v_lshl_add_u32 v242, v243, 8, v242
	v_lshl_add_u32 v242, s0, 12, v242
	v_lshl_add_u32 v242, s16, 12, v242
	v_add_u32_e32 v242, 0x8000, v242
	v_mov_b32_e32 v243, s8
	v_bfe_u32 v244, v243, 2, 2
	v_lshl_add_u32 v242, v244, 10, v242
	v_bfe_u32 v244, v243, 1, 1
	v_lshl_add_u32 v242, v244, 9, v242
	v_mov_b32_e32 v243, 0
	v_mov_b64_e32 v[2:3], s[62:63]
	s_movk_i32 s7, 0x2900
	v_mad_i64_i32 v[2:3], s[14:15], v92, s7, v[2:3]
	s_lshl_b32 s14, s8, 6
	s_lshl_b32 s1, s9, 7
	s_and_b32 s14, s14, 64
	v_and_b32_e32 v136, 15, v0
	s_or_b32 s1, s14, s1
	s_lshl_b32 s12, s8, 3
	v_or_b32_e32 v4, s1, v136
	v_lshrrev_b32_e32 v246, 4, v0
	v_lshlrev_b32_e32 v246, 8, v246
	v_lshl_add_u32 v246, v136, 4, v246
	v_lshl_add_u32 v246, s1, 15, v246
	v_lshl_add_u32 v246, s0, 5, v246
	v_mov_b32_e32 v247, 0
	s_waitcnt lgkmcnt(0)
	v_ashrrev_i32_e32 v1, 4, v0
	s_and_b32 s12, s12, 0x70
	v_mul_u32_u24_e32 v4, 0x4080, v4
	v_lshlrev_b32_e32 v0, 4, v0
	s_movk_i32 s15, 0x120
	s_lshl_b32 s96, s9, 8
	v_lshlrev_b32_e32 v84, 1, v4
	v_mov_b32_e32 v85, v185
	s_ashr_i32 s1, s0, 31
	v_lshlrev_b32_e32 v86, 3, v1
	v_lshlrev_b32_e32 v138, 2, v1
	v_and_b32_e32 v80, 16, v0
	v_mul_lo_u32 v7, v1, s15
	v_lshl_add_u64 v[0:1], v[2:3], 0, s[96:97]
	s_lshl_b32 s96, s12, 1
	v_lshl_add_u64 v[4:5], s[62:63], 0, v[84:85]
	v_ashrrev_i32_e32 v87, 31, v86
	v_lshl_add_u64 v[0:1], v[0:1], 0, s[96:97]
	v_mov_b32_e32 v81, v185
	s_lshl_b64 s[0:1], s[0:1], 1
	v_lshl_add_u64 v[16:17], v[0:1], 0, v[80:81]
	v_lshl_add_u64 v[16:17], s[62:63], 0, v[242:243]
	v_lshl_add_u64 v[0:1], v[4:5], 0, s[0:1]
	v_lshlrev_b64 v[88:89], 1, v[86:87]
	v_lshl_add_u64 v[18:19], v[0:1], 0, v[88:89]
	v_lshl_add_u64 v[18:19], s[62:63], 0, v[246:247]
	v_sub_u32_e32 v1, 63, v86
	v_cvt_f32_i32_e32 v1, v1
	v_readlane_b32 s6, v253, 48
	s_mov_b64 s[18:19], 0x30c00000
	s_waitcnt vmcnt(0)
	v_lshl_add_u64 v[44:45], v[18:19], 0, s[18:19]
	v_mov_b32_e32 v0, s6
	v_mad_u64_u32 v[90:91], s[18:19], v6, 36, v[0:1]
	v_mul_f32_e32 v0, v82, v1
	v_sub_u32_e32 v1, 62, v86
	v_cvt_f32_i32_e32 v1, v1
	v_sub_u32_e32 v2, 61, v86
	v_cvt_f32_i32_e32 v2, v2
	v_exp_f32_e32 v140, v0
	v_mul_f32_e32 v0, v82, v1
	v_sub_u32_e32 v1, 60, v86
	v_cvt_f32_i32_e32 v1, v1
	v_exp_f32_e32 v142, v0
	v_mul_f32_e32 v0, v82, v2
	s_mov_b32 s15, 0xdfff800
	v_exp_f32_e32 v141, v0
	v_mul_f32_e32 v0, v82, v1
	v_add_co_u32_e32 v24, vcc, s15, v16
	v_exp_f32_e32 v143, v0
	v_sub_u32_e32 v0, 58, v86
	v_addc_co_u32_e32 v25, vcc, 0, v17, vcc
	s_mov_b32 s15, 0xe01f800
	v_cvt_f32_i32_e32 v91, v0
	v_add_co_u32_e32 v0, vcc, s15, v16
	s_mov_b32 s15, 0x30c00000
	s_nop 0
	v_addc_co_u32_e32 v1, vcc, 0, v17, vcc
	v_add_co_u32_e32 v4, vcc, s15, v18
	s_mov_b32 s15, 0x30c80000
	s_nop 0
	v_addc_co_u32_e32 v5, vcc, 0, v19, vcc
	v_add_co_u32_e32 v60, vcc, s15, v18
	s_mov_b32 s15, 0x30d00000
	s_nop 0
	v_addc_co_u32_e32 v61, vcc, 0, v19, vcc
	v_add_co_u32_e32 v68, vcc, s15, v18
	s_mov_b32 s15, 0x30d80000
	s_nop 0
	v_addc_co_u32_e32 v69, vcc, 0, v19, vcc
	v_add_co_u32_e32 v76, vcc, s15, v18
	v_sub_u32_e32 v2, 59, v86
	s_nop 0
	v_addc_co_u32_e32 v77, vcc, 0, v19, vcc
	s_mov_b32 s15, 0xe03f800
	v_cvt_f32_i32_e32 v2, v2
	v_add_co_u32_e32 v18, vcc, s15, v16
	s_mov_b32 s15, 0xe05f800
	s_nop 0
	v_addc_co_u32_e32 v19, vcc, 0, v17, vcc
	v_add_co_u32_e32 v20, vcc, s15, v16
	v_add_u32_e32 v81, s6, v7
	s_nop 0
	v_addc_co_u32_e32 v21, vcc, 0, v17, vcc
	v_mul_f32_e32 v87, v82, v2
	global_load_dwordx4 v[0:3], v[0:1], off offset:2048
	s_nop 0
	global_load_dwordx4 v[4:7], v[4:5], off
	s_nop 0
	global_load_dwordx4 v[8:11], v[60:61], off
	s_waitcnt lgkmcnt(0)
; __device__ __forceinline__ float fexp2(float x) { return __builtin_amdgcn_exp2f(x); }
; __device__ __forceinline__ void scan_load(ScanOps& o, const bf16* kg, const bf16* vrow, int n) {
; #pragma unroll
;     for (int i = 0; i < 2; ++i) o.kp[i] = ld_u4(kg + (size_t)(n * CH + i * 32) * TOKP);
; #pragma unroll
;     for (int eb = 0; eb < 4; ++eb)
; #pragma unroll
;         for (int ks = 0; ks < 2; ++ks) o.va[eb][ks] = ld_b8(vrow + (size_t)eb * 16 * SWPP + n * CH + ks * 32);
; }
; __device__ __forceinline__ void scan_task(const Frame& F, int task) {
;     ...
;     const float lg = pg8::lg2gamma(h), cd = fexp2(64.f * lg);
;     float dec[16];
; #pragma unroll
;     for (int i = 0; i < 16; ++i) dec[i] = fexp2((float)(63 - ((i >> 3) * 32 + rq * 8 + (i & 7))) * lg);
;     ScanOps o0, o1, o2;
;     scan_load(o0, kg, vrow, 0); scan_load(o1, kg, vrow, 1);
	global_load_dwordx4 v[12:15], v[60:61], off offset:1024
	global_load_dwordx4 v[28:31], v[68:69], off
	global_load_dwordx4 v[32:35], v[68:69], off offset:1024
	global_load_dwordx4 v[48:51], v[76:77], off
	global_load_dwordx4 v[52:55], v[76:77], off offset:1024
	s_nop 0
	global_load_dwordx4 v[16:19], v[18:19], off offset:2048
	s_nop 0
	global_load_dwordx4 v[20:23], v[20:21], off offset:2048
	s_nop 0
	global_load_dwordx4 v[40:43], v[44:45], off offset:1024
	global_load_dwordx4 v[36:39], v[44:45], off offset:2048
	s_nop 0
	global_load_dwordx4 v[24:27], v[24:25], off offset:2048
	s_nop 0
	global_load_dwordx4 v[44:47], v[44:45], off offset:3072
	s_nop 0
	global_load_dwordx4 v[56:59], v[60:61], off offset:2048
	s_nop 0
	global_load_dwordx4 v[60:63], v[60:61], off offset:3072
	s_nop 0
	global_load_dwordx4 v[64:67], v[68:69], off offset:2048
	s_nop 0
	global_load_dwordx4 v[68:71], v[68:69], off offset:3072
	s_nop 0
	global_load_dwordx4 v[72:75], v[76:77], off offset:2048
	s_nop 0
	global_load_dwordx4 v[76:79], v[76:77], off offset:3072
	v_exp_f32_e32 v144, v87
	v_mul_f32_e32 v87, v82, v91
	v_sub_u32_e32 v91, 57, v86
	v_cvt_f32_i32_e32 v91, v91
	v_sub_u32_e32 v94, 56, v86
	v_cvt_f32_i32_e32 v94, v94
	v_exp_f32_e32 v146, v87
	v_mul_f32_e32 v87, v82, v91
	v_sub_u32_e32 v91, 31, v86
	v_cvt_f32_i32_e32 v91, v91
	v_exp_f32_e32 v145, v87
	v_mul_f32_e32 v87, v82, v94
	v_sub_u32_e32 v94, 30, v86
	v_cvt_f32_i32_e32 v94, v94
	v_exp_f32_e32 v147, v87
	v_mul_f32_e32 v87, v82, v91
	v_sub_u32_e32 v91, 29, v86
	v_cvt_f32_i32_e32 v91, v91
	v_exp_f32_e32 v148, v87
	v_mul_f32_e32 v87, v82, v94
	v_sub_u32_e32 v94, 28, v86
	v_cvt_f32_i32_e32 v94, v94
	v_exp_f32_e32 v150, v87
	v_mul_f32_e32 v87, v82, v91
	v_sub_u32_e32 v91, 27, v86
	v_cvt_f32_i32_e32 v91, v91
	v_exp_f32_e32 v149, v87
	v_mul_f32_e32 v87, v82, v94
	v_sub_u32_e32 v94, 26, v86
	v_cvt_f32_i32_e32 v94, v94
	v_exp_f32_e32 v151, v87
	v_mul_f32_e32 v87, v82, v91
	v_sub_u32_e32 v91, 25, v86
	v_sub_u32_e32 v86, 24, v86
	v_cvt_f32_i32_e32 v91, v91
	v_cvt_f32_i32_e32 v86, v86
	v_exp_f32_e32 v152, v87
	v_mul_f32_e32 v87, v82, v94
	v_mul_f32_e32 v83, 0x42800000, v82
	v_exp_f32_e32 v154, v87
	v_mul_f32_e32 v87, v82, v91
	v_mul_f32_e32 v82, v82, v86
	v_exp_f32_e32 v156, v83
	v_exp_f32_e32 v155, v82
	v_lshl_add_u64 v[82:83], s[0:1], 0, v[88:89]
	s_or_b32 s0, s13, s16
	s_ashr_i32 s1, s0, 31
	s_and_b32 s5, s3, 64
	s_lshl_b64 s[0:1], s[0:1], 12
	s_or_b32 s0, s0, s5
	v_exp_f32_e32 v153, v87
	v_lshl_add_u64 v[160:161], v[82:83], 0, v[84:85]
	v_mov_b32_e32 v160, v246
	v_mov_b32_e32 v161, 0
	v_mov_b32_e32 v82, s0
	v_mov_b32_e32 v83, s1
	v_lshlrev_b64 v[82:83], 8, v[82:83]
	v_ashrrev_i32_e32 v139, 31, v138
	v_lshlrev_b32_e32 v93, 1, v136
	v_lshl_or_b32 v82, s4, 4, v82
	v_mad_i64_i32 v[164:165], s[0:1], v92, s7, v[184:185]
	v_mov_b32_e32 v88, 0
	s_mov_b32 s15, 0
	v_mov_b32_e32 v158, v156
	v_mov_b32_e32 v159, v156
	v_and_b32_e32 v240, 8, v138
	v_and_b32_e32 v241, 4, v138
	v_lshlrev_b32_e32 v240, 5, v240
	v_lshl_or_b32 v240, v241, 1, v240
	v_lshl_or_b32 v240, v136, 4, v240
	v_mov_b32_e32 v241, 0
	v_lshl_add_u64 v[162:163], v[82:83], 0, v[240:241]
	v_or3_b32 v164, v164, s4, v80
	v_mov_b32_e32 v164, v242
	v_mov_b32_e32 v165, 0
	v_add_u32_e32 v137, v90, v80
	v_add_u32_e32 v168, v81, v93
	v_mov_b32_e32 v89, v88
	v_mov_b32_e32 v90, v88
	v_mov_b32_e32 v91, v88
	v_mov_b32_e32 v92, v88
	v_mov_b32_e32 v93, v88
	v_mov_b32_e32 v94, v88
	v_mov_b32_e32 v95, v88
	v_mov_b32_e32 v84, v88
	v_mov_b32_e32 v85, v88
	v_mov_b32_e32 v86, v88
	v_mov_b32_e32 v87, v88
	v_mov_b32_e32 v80, v88
	v_mov_b32_e32 v81, v88
	v_mov_b32_e32 v82, v88
	v_mov_b32_e32 v83, v88
	s_branch .LBB0_507

; #define LAS __attribute__((address_space(3)))
; #define LDS_WAIT() asm volatile("s_waitcnt lgkmcnt(0)" ::: "memory")
; __device__ __forceinline__ unsigned pk2(float lo, float hi) { return f2bf(lo) | (f2bf(hi) << 16); }
; __device__ __forceinline__ void scan_load(ScanOps& o, const bf16* kg, const bf16* vrow, int n) {
; #pragma unroll
;     for (int i = 0; i < 2; ++i) o.kp[i] = ld_u4(kg + (size_t)(n * CH + i * 32) * TOKP);
; #pragma unroll
;     for (int eb = 0; eb < 4; ++eb)
; #pragma unroll
;         for (int ks = 0; ks < 2; ++ks) o.va[eb][ks] = ld_b8(vrow + (size_t)eb * 16 * SWPP + n * CH + ks * 32);
; }
; __device__ __forceinline__ void scan_step(f32x4 (&st)[4], const ScanOps& o, const float (&dec)[16], LAS unsigned char* kw, const LAS unsigned char* kr, bf16* sp, int n, float cd) {
; #pragma unroll
;     for (int eb = 0; eb < 4; ++eb) { u32x2 w; w.x = pk2(st[eb][0], st[eb][1]); w.y = pk2(st[eb][2], st[eb][3]); st_u2(sp + (size_t)n * HD * HD + eb * 16 * HD, w); }
; #pragma unroll
;     for (int i = 0; i < 2; ++i)
; #pragma unroll
;         for (int d = 0; d < 4; ++d) *(LAS unsigned*)(kw + i * 32 * SC_PITCH + d * 4) = o.kp[i][d];
;     LDS_WAIT(); asm volatile("" ::: "memory");
;     bf16x8 ka[2];
; #pragma unroll
;     for (int ks = 0; ks < 2; ++ks) { u32x4 w;
; #pragma unroll
;         for (int j = 0; j < 4; ++j) { const unsigned e0 = *(const LAS unsigned short*)(kr + (ks * 32 + 2 * j) * SC_PITCH), e1 = *(const LAS unsigned short*)(kr + (ks * 32 + 2 * j + 1) * SC_PITCH);
;             w[j] = pk2(bf_lo(e0) * dec[ks * 8 + 2 * j], bf_lo(e1) * dec[ks * 8 + 2 * j + 1]); }
;         ka[ks] = __builtin_bit_cast(bf16x8, w); }
.LBB0_506:
	s_mov_b64 s[0:1], 0x1800
	v_lshl_add_u64 v[160:161], v[160:161], 0, s[0:1]
	s_mov_b64 s[0:1], 0x18000
	s_add_i32 s4, s15, 3
	v_lshl_add_u64 v[162:163], v[162:163], 0, s[0:1]
	s_mov_b64 s[0:1], 0xc0000
	v_lshl_add_u64 v[164:165], v[164:165], 0, s[0:1]
	s_cmp_lt_u32 s15, 28
	s_mov_b32 s15, s4
	s_cbranch_scc0 .LBB0_482
.LBB0_507:
	s_cmp_lt_u32 s15, 29
	s_cselect_b64 s[0:1], -1, 0
	s_cmp_gt_u32 s15, 28
	s_cbranch_scc1 .LBB0_509
	v_lshl_add_u64 v[96:97], s[62:63], 0, v[164:165]
	v_add_co_u32_e32 v98, vcc, 0xe07f800, v96
	s_waitcnt vmcnt(5)
	v_lshl_add_u64 v[128:129], s[62:63], 0, v[160:161]
	v_addc_co_u32_e32 v99, vcc, 0, v97, vcc
	v_add_co_u32_e32 v100, vcc, 0xe09f800, v96
	s_nop 1
	v_addc_co_u32_e32 v101, vcc, 0, v97, vcc
	v_add_co_u32_e32 v108, vcc, 0x30c01000, v128
	global_load_dwordx4 v[96:99], v[98:99], off offset:2048
	s_nop 0
	global_load_dwordx4 v[100:103], v[100:101], off offset:2048
	v_addc_co_u32_e32 v109, vcc, 0, v129, vcc
	v_add_co_u32_e32 v116, vcc, 0x30c81000, v128
	global_load_dwordx4 v[104:107], v[108:109], off
	s_nop 0
	global_load_dwordx4 v[108:111], v[108:109], off offset:1024
	v_addc_co_u32_e32 v117, vcc, 0, v129, vcc
	v_add_co_u32_e32 v124, vcc, 0x30d01000, v128
	global_load_dwordx4 v[112:115], v[116:117], off
	s_nop 0
	global_load_dwordx4 v[116:119], v[116:117], off offset:1024
	v_addc_co_u32_e32 v125, vcc, 0, v129, vcc
	s_waitcnt vmcnt(10)
	v_add_co_u32_e32 v132, vcc, 0x30d81000, v128
	global_load_dwordx4 v[120:123], v[124:125], off
	s_nop 0
	global_load_dwordx4 v[124:127], v[124:125], off offset:1024
	v_addc_co_u32_e32 v133, vcc, 0, v129, vcc
	global_load_dwordx4 v[128:131], v[132:133], off
	s_nop 0
	global_load_dwordx4 v[132:135], v[132:133], off offset:1024
.LBB0_509:
	s_nop 4
	v_cvt_pk_bf16_f32 v170, v88, v89
	s_nop 4
	v_lshl_add_u64 v[166:167], s[62:63], 0, v[162:163]
	v_cvt_pk_bf16_f32 v171, v90, v91
	s_mov_b32 s4, 0x22c01000
	s_nop 0
	v_add_co_u32_e32 v172, vcc, s4, v166
	s_nop 1
	v_addc_co_u32_e32 v173, vcc, 0, v167, vcc
	s_nop 1
	global_store_dwordx2 v[172:173], v[170:171], off offset:-4096
	v_cvt_pk_bf16_f32 v170, v92, v93
	s_nop 4
	v_cvt_pk_bf16_f32 v171, v94, v95
	s_nop 4
	global_store_dwordx2 v[172:173], v[170:171], off
	v_cvt_pk_bf16_f32 v170, v84, v85
	s_nop 4
	v_cvt_pk_bf16_f32 v171, v86, v87
	s_mov_b32 s4, 0x22c03000
	s_nop 0
	v_add_co_u32_e32 v172, vcc, s4, v166
	s_nop 1
	v_addc_co_u32_e32 v173, vcc, 0, v167, vcc
	s_nop 1
	global_store_dwordx2 v[172:173], v[170:171], off offset:-4096
	v_cvt_pk_bf16_f32 v170, v80, v81
	s_nop 4
	v_cvt_pk_bf16_f32 v171, v82, v83
	global_store_dwordx2 v[172:173], v[170:171], off
	v_add_u32_e32 v169, 0x480, v137
	v_add_u32_e32 v170, 0x488, v137
	s_waitcnt vmcnt(11)
	ds_write2_b32 v137, v24, v25 offset1:1
	ds_write2_b32 v137, v26, v27 offset0:2 offset1:3
	ds_write2_b32 v169, v0, v1 offset1:1
	ds_write2_b32 v170, v2, v3 offset1:1
	s_waitcnt lgkmcnt(0)
	ds_read_u16 v157, v168 offset:72
	ds_read_u16 v171, v168 offset:108
	ds_read_u16 v172, v168
	ds_read_u16 v176, v168 offset:144
	ds_read_u16 v177, v168 offset:216
	ds_read_u16 v178, v168 offset:252
	ds_read_u16 v179, v168 offset:180
	ds_read_u16 v174, v168 offset:36
	s_waitcnt lgkmcnt(7)
	v_lshlrev_b32_e32 v173, 16, v157
	s_waitcnt lgkmcnt(5)
	v_lshlrev_b32_e32 v172, 16, v172
	v_pk_mul_f32 v[172:173], v[140:141], v[172:173]
	v_lshlrev_b32_e32 v175, 16, v171
	v_and_b32_sdwa v157, v173, v213 dst_sel:DWORD dst_unused:UNUSED_PAD src0_sel:WORD_1 src1_sel:DWORD
	v_and_b32_sdwa v171, v172, v213 dst_sel:DWORD dst_unused:UNUSED_PAD src0_sel:WORD_1 src1_sel:DWORD
	v_add3_u32 v157, v173, v157, s76
	v_add3_u32 v171, v172, v171, s76
	s_waitcnt lgkmcnt(3)
	v_lshlrev_b32_e32 v173, 16, v177
	v_lshlrev_b32_e32 v172, 16, v176
	s_waitcnt lgkmcnt(0)
	v_lshlrev_b32_e32 v174, 16, v174
	v_pk_mul_f32 v[172:173], v[144:145], v[172:173]
	v_lshlrev_b32_e32 v177, 16, v178
	v_lshlrev_b32_e32 v176, 16, v179
	v_pk_mul_f32 v[174:175], v[142:143], v[174:175]
	v_pk_mul_f32 v[176:177], v[146:147], v[176:177]
	v_and_b32_sdwa v178, v173, v213 dst_sel:DWORD dst_unused:UNUSED_PAD src0_sel:WORD_1 src1_sel:DWORD
	v_and_b32_sdwa v179, v172, v213 dst_sel:DWORD dst_unused:UNUSED_PAD src0_sel:WORD_1 src1_sel:DWORD
	v_add3_u32 v182, v173, v178, s76
	v_add3_u32 v172, v172, v179, s76
	v_bfe_u32 v173, v176, 16, 1
	v_bfe_u32 v178, v175, 16, 1
	v_bfe_u32 v179, v174, 16, 1
	v_bfe_u32 v180, v177, 16, 1
	v_lshrrev_b32_e32 v171, 16, v171
	v_lshrrev_b32_e32 v157, 16, v157
	v_lshrrev_b32_e32 v172, 16, v172
	v_add3_u32 v183, v177, v180, s76
	v_add3_u32 v177, v174, v179, s76
	v_add3_u32 v175, v175, v178, s76
	v_add3_u32 v173, v176, v173, s76
	v_and_or_b32 v174, v173, s75, v172
	v_and_or_b32 v173, v175, s75, v157
	v_and_or_b32 v172, v177, s75, v171
	ds_read_u16 v157, v168 offset:1152
	ds_read_u16 v171, v168 offset:1224
	ds_read_u16 v175, v168 offset:1260
	ds_read_u16 v180, v168 offset:1296
	ds_read_u16 v181, v168 offset:1368
	ds_read_u16 v184, v168 offset:1404
	ds_read_u16 v194, v168 offset:1332
	ds_read_u16 v178, v168 offset:1188
	s_waitcnt lgkmcnt(6)
; #define LAS __attribute__((address_space(3)))
; #define LDS_WAIT() asm volatile("s_waitcnt lgkmcnt(0)" ::: "memory")
; __device__ __forceinline__ unsigned pk2(float lo, float hi) { return f2bf(lo) | (f2bf(hi) << 16); }
; __device__ __forceinline__ f32x4 mfma16(bf16x8 a, bf16x8 b, f32x4 c) { return __builtin_amdgcn_mfma_f32_16x16x32_bf16(a, b, c, 0, 0, 0); }
; __device__ __forceinline__ void scan_load(ScanOps& o, const bf16* kg, const bf16* vrow, int n) {
; #pragma unroll
;     for (int i = 0; i < 2; ++i) o.kp[i] = ld_u4(kg + (size_t)(n * CH + i * 32) * TOKP);
; #pragma unroll
;     for (int eb = 0; eb < 4; ++eb)
; #pragma unroll
;         for (int ks = 0; ks < 2; ++ks) o.va[eb][ks] = ld_b8(vrow + (size_t)eb * 16 * SWPP + n * CH + ks * 32);
; }
; __device__ __forceinline__ void scan_step(f32x4 (&st)[4], const ScanOps& o, const float (&dec)[16], LAS unsigned char* kw, const LAS unsigned char* kr, bf16* sp, int n, float cd) {
; #pragma unroll
;     for (int eb = 0; eb < 4; ++eb) { u32x2 w; w.x = pk2(st[eb][0], st[eb][1]); w.y = pk2(st[eb][2], st[eb][3]); st_u2(sp + (size_t)n * HD * HD + eb * 16 * HD, w); }
; #pragma unroll
;     for (int i = 0; i < 2; ++i)
; #pragma unroll
;         for (int d = 0; d < 4; ++d) *(LAS unsigned*)(kw + i * 32 * SC_PITCH + d * 4) = o.kp[i][d];
;     LDS_WAIT(); asm volatile("" ::: "memory");
;     bf16x8 ka[2];
; #pragma unroll
;     for (int ks = 0; ks < 2; ++ks) { u32x4 w;
; #pragma unroll
;         for (int j = 0; j < 4; ++j) { const unsigned e0 = *(const LAS unsigned short*)(kr + (ks * 32 + 2 * j) * SC_PITCH), e1 = *(const LAS unsigned short*)(kr + (ks * 32 + 2 * j + 1) * SC_PITCH);
;             w[j] = pk2(bf_lo(e0) * dec[ks * 8 + 2 * j], bf_lo(e1) * dec[ks * 8 + 2 * j + 1]); }
;         ka[ks] = __builtin_bit_cast(bf16x8, w); }
;     LDS_WAIT(); asm volatile("" ::: "memory");
; #pragma unroll
;     for (int eb = 0; eb < 4; ++eb) { st[eb] *= cd;
; #pragma unroll
;         for (int ks = 0; ks < 2; ++ks) st[eb] = mfma16(ka[ks], o.va[eb][ks], st[eb]); }
	v_lshlrev_b32_e32 v177, 16, v171
	v_lshlrev_b32_e32 v176, 16, v157
	v_pk_mul_f32 v[176:177], v[148:149], v[176:177]
	s_waitcnt lgkmcnt(5)
	v_lshlrev_b32_e32 v179, 16, v175
	v_and_b32_sdwa v157, v177, v213 dst_sel:DWORD dst_unused:UNUSED_PAD src0_sel:WORD_1 src1_sel:DWORD
	v_and_b32_sdwa v171, v176, v213 dst_sel:DWORD dst_unused:UNUSED_PAD src0_sel:WORD_1 src1_sel:DWORD
	v_add3_u32 v157, v177, v157, s76
	v_add3_u32 v171, v176, v171, s76
	s_waitcnt lgkmcnt(3)
	v_lshlrev_b32_e32 v177, 16, v181
	v_lshlrev_b32_e32 v176, 16, v180
	v_pk_mul_f32 v[176:177], v[152:153], v[176:177]
	s_waitcnt lgkmcnt(2)
	v_lshlrev_b32_e32 v181, 16, v184
	s_waitcnt lgkmcnt(1)
	v_lshlrev_b32_e32 v180, 16, v194
	s_waitcnt lgkmcnt(0)
	v_lshlrev_b32_e32 v178, 16, v178
	v_pk_mul_f32 v[180:181], v[154:155], v[180:181]
	v_and_b32_sdwa v175, v177, v213 dst_sel:DWORD dst_unused:UNUSED_PAD src0_sel:WORD_1 src1_sel:DWORD
	v_and_b32_sdwa v184, v176, v213 dst_sel:DWORD dst_unused:UNUSED_PAD src0_sel:WORD_1 src1_sel:DWORD
	v_pk_mul_f32 v[178:179], v[150:151], v[178:179]
	v_add3_u32 v194, v177, v175, s76
	v_add3_u32 v175, v176, v184, s76
	v_bfe_u32 v176, v180, 16, 1
	v_lshrrev_b32_e32 v175, 16, v175
	v_bfe_u32 v184, v178, 16, 1
	v_add3_u32 v176, v180, v176, s76
	v_add3_u32 v184, v178, v184, s76
	v_and_or_b32 v178, v176, s75, v175
	v_perm_b32 v175, v183, v182, s71
	v_bfe_u32 v177, v179, 16, 1
	v_lshrrev_b32_e32 v157, 16, v157
	v_bfe_u32 v195, v181, 16, 1
	v_add3_u32 v177, v179, v177, s76
	v_lshrrev_b32_e32 v171, 16, v171
	v_add3_u32 v181, v181, v195, s76
	v_and_or_b32 v177, v177, s75, v157
	v_mov_b32_e32 v157, v156
	v_and_or_b32 v176, v184, s75, v171
	v_pk_mul_f32 v[90:91], v[156:157], v[90:91]
	v_pk_mul_f32 v[88:89], v[158:159], v[88:89]
	v_perm_b32 v179, v181, v194, s71
	v_pk_mul_f32 v[94:95], v[156:157], v[94:95]
	v_pk_mul_f32 v[92:93], v[158:159], v[92:93]
	v_pk_mul_f32 v[86:87], v[156:157], v[86:87]
	v_pk_mul_f32 v[84:85], v[158:159], v[84:85]
	v_pk_mul_f32 v[82:83], v[156:157], v[82:83]
	v_pk_mul_f32 v[80:81], v[158:159], v[80:81]
	v_mfma_f32_16x16x32_bf16 v[88:91], v[172:175], v[4:7], v[88:91]
	s_waitcnt lgkmcnt(0)
	s_cmp_eq_u32 s15, 30
	v_mfma_f32_16x16x32_bf16 v[92:95], v[172:175], v[8:11], v[92:95]
	v_mfma_f32_16x16x32_bf16 v[84:87], v[172:175], v[28:31], v[84:87]
	s_waitcnt vmcnt(9)
	v_mfma_f32_16x16x32_bf16 v[80:83], v[172:175], v[48:51], v[80:83]
	v_mfma_f32_16x16x32_bf16 v[88:91], v[176:179], v[40:43], v[88:91]
	v_mfma_f32_16x16x32_bf16 v[92:95], v[176:179], v[12:15], v[92:95]
	v_mfma_f32_16x16x32_bf16 v[84:87], v[176:179], v[32:35], v[84:87]
	s_waitcnt vmcnt(8)
	v_mfma_f32_16x16x32_bf16 v[80:83], v[176:179], v[52:55], v[80:83]
	s_cbranch_scc1 .LBB0_513
	s_cmp_gt_u32 s15, 27
	s_cbranch_scc1 .LBB0_512
	v_lshl_add_u64 v[0:1], s[62:63], 0, v[164:165]
	v_add_co_u32_e32 v2, vcc, 0xe0bf800, v0
	v_lshl_add_u64 v[48:49], s[62:63], 0, v[160:161]
	s_nop 0
	v_addc_co_u32_e32 v3, vcc, 0, v1, vcc
	v_add_co_u32_e32 v0, vcc, 0xe0df800, v0
	s_nop 1
	v_addc_co_u32_e32 v1, vcc, 0, v1, vcc
	v_add_co_u32_e32 v8, vcc, 0x30c01800, v48
	global_load_dwordx4 v[24:27], v[2:3], off offset:2048
	s_nop 0
	global_load_dwordx4 v[0:3], v[0:1], off offset:2048
	v_addc_co_u32_e32 v9, vcc, 0, v49, vcc
	v_add_co_u32_e32 v12, vcc, 0x30c81800, v48
	global_load_dwordx4 v[4:7], v[8:9], off
	global_load_dwordx4 v[40:43], v[8:9], off offset:1024
	v_addc_co_u32_e32 v13, vcc, 0, v49, vcc
	v_add_co_u32_e32 v32, vcc, 0x30d01800, v48
	global_load_dwordx4 v[8:11], v[12:13], off
	s_nop 0
	global_load_dwordx4 v[12:15], v[12:13], off offset:1024
	v_addc_co_u32_e32 v33, vcc, 0, v49, vcc
	v_add_co_u32_e32 v52, vcc, 0x30d81800, v48
	global_load_dwordx4 v[28:31], v[32:33], off
	s_nop 0
	global_load_dwordx4 v[32:35], v[32:33], off offset:1024
	v_addc_co_u32_e32 v53, vcc, 0, v49, vcc
	global_load_dwordx4 v[48:51], v[52:53], off
	s_nop 0
	global_load_dwordx4 v[52:55], v[52:53], off offset:1024

; __device__ __forceinline__ void scan_load(ScanOps& o, const bf16* kg, const bf16* vrow, int n) {
; #pragma unroll
;     for (int i = 0; i < 2; ++i) o.kp[i] = ld_u4(kg + (size_t)(n * CH + i * 32) * TOKP);
; #pragma unroll
;     for (int eb = 0; eb < 4; ++eb)
; #pragma unroll
;         for (int ks = 0; ks < 2; ++ks) o.va[eb][ks] = ld_b8(vrow + (size_t)eb * 16 * SWPP + n * CH + ks * 32);
; }
; __device__ __forceinline__ void scan_task(const Frame& F, int task) {
;     ...
;         if (n + 2 < NCH - 1) { if (n + 4 < NCH - 1) scan_load(o1, kg, vrow, n + 4); scan_step(st, o2, dec, kw, kr, sp, n + 2, cd); }
.LBB0_513:
	s_andn2_b64 vcc, exec, s[0:1]
	s_cbranch_vccnz .LBB0_506
	s_cmp_gt_u32 s15, 26
	s_cbranch_scc1 .LBB0_505
	v_lshl_add_u64 v[16:17], s[62:63], 0, v[164:165]
	v_add_co_u32_e32 v18, vcc, 0xe0ff800, v16
	s_waitcnt vmcnt(5)
	v_lshl_add_u64 v[72:73], s[62:63], 0, v[160:161]
	v_addc_co_u32_e32 v19, vcc, 0, v17, vcc
	v_add_co_u32_e32 v20, vcc, 0xe11f800, v16
	s_nop 1
	v_addc_co_u32_e32 v21, vcc, 0, v17, vcc
	v_add_co_u32_e32 v44, vcc, 0x30c02000, v72
	global_load_dwordx4 v[16:19], v[18:19], off offset:2048
	s_nop 0
	global_load_dwordx4 v[20:23], v[20:21], off offset:2048
	v_addc_co_u32_e32 v45, vcc, 0, v73, vcc
	v_add_co_u32_e32 v60, vcc, 0x30c82000, v72
	global_load_dwordx4 v[36:39], v[44:45], off
	s_nop 0
	global_load_dwordx4 v[44:47], v[44:45], off offset:1024
	v_addc_co_u32_e32 v61, vcc, 0, v73, vcc
	v_add_co_u32_e32 v68, vcc, 0x30d02000, v72
	global_load_dwordx4 v[56:59], v[60:61], off
	s_nop 0
	global_load_dwordx4 v[60:63], v[60:61], off offset:1024
	v_addc_co_u32_e32 v69, vcc, 0, v73, vcc
	s_waitcnt vmcnt(10)
	v_add_co_u32_e32 v76, vcc, 0x30d82000, v72
	global_load_dwordx4 v[64:67], v[68:69], off
	s_nop 0
	global_load_dwordx4 v[68:71], v[68:69], off offset:1024
	v_addc_co_u32_e32 v77, vcc, 0, v73, vcc
	global_load_dwordx4 v[72:75], v[76:77], off
	s_nop 0
	global_load_dwordx4 v[76:79], v[76:77], off offset:1024
	s_branch .LBB0_505

; __device__ __forceinline__ f32x4 mfma16(bf16x8 a, bf16x8 b, f32x4 c) { return __builtin_amdgcn_mfma_f32_16x16x32_bf16(a, b, c, 0, 0, 0); }
; __device__ __forceinline__ void ret_task(const Frame& F, int l, int task) {
;     ...
;     const int qb2 = task & 1, n = (task >> 1) & 31, h = (task >> 6) & 7, b = task >> 9, bhh = b * NH + h;
;     const bf16* TOK = (const bf16*)(F.ws + WS_TOK); const bf16* SWP = (const bf16*)(F.ws + WS_SWP); const bf16* ST = (const bf16*)(F.ws + WS_ST);
;     bf16* MIX = (bf16*)(F.ws + WS_MIX);
;     const int tc0 = b * S + n * CH, tq0 = tc0 + qb2 * 32;
;     const float lg = pg8::lg2gamma(h);
;     bf16x8 Qf[2][4], Kf[2][2][4];
; #pragma unroll
;     for (int qb = 0; qb < 2; ++qb)
; #pragma unroll
;         for (int ks = 0; ks < 4; ++ks) Qf[qb][ks] = ld_b8(TOK + (size_t)(tq0 + qb * 16 + c) * TOKP + TK_QR + h * HD + ks * 32 + rq * 8);
; #pragma unroll
;     for (int g = 0; g < 2; ++g)
; #pragma unroll
;         for (int ab = 0; ab < 2; ++ab) { const int key = 32 * g + (c >> 2) * 8 + 4 * ab + (c & 3);
; #pragma unroll
;             for (int ks = 0; ks < 4; ++ks) Kf[g][ab][ks] = ld_b8(TOK + (size_t)(tc0 + key) * TOKP + TK_KR + h * HD + rq * 8 + ks * 32); }
;     f32x4 acc[2][8];
; #pragma unroll
;     for (int qb = 0; qb < 2; ++qb)
; #pragma unroll
;         for (int eb = 0; eb < 8; ++eb) acc[qb][eb] = (f32x4){0.f, 0.f, 0.f, 0.f};
;     const bf16* sp = ST + (((size_t)bhh * NCH + n) * HD + c) * HD + rq * 8;
; #pragma unroll
;     for (int eb = 0; eb < 8; ++eb)
; #pragma unroll
;         for (int ks = 0; ks < 4; ++ks) { const bf16x8 sf = ld_b8(sp + eb * 16 * HD + ks * 32);
; #pragma unroll
;             for (int qb = 0; qb < 2; ++qb) acc[qb][eb] = mfma16(sf, Qf[qb][ks], acc[qb][eb]); }
.LBB0_655:
	s_bfe_u32 s1, s8, 0x50001
	s_ashr_i32 s0, s8, 9
	s_lshl_b32 s4, s0, 3
	s_lshl_b32 s0, s0, 11
	s_lshl_b32 s5, s1, 6
	v_and_b32_e32 v180, 15, v118
	s_or_b32 s0, s5, s0
	v_readlane_b32 s5, v251, 32
	v_ashrrev_i32_e32 v205, 4, v118
	s_or_b32 s4, s4, s9
	v_or_b32_e32 v209, s5, v180
	v_or_b32_e32 v196, s0, v209
	v_lshlrev_b32_e32 v202, 3, v205
	v_mov_b64_e32 v[160:161], s[80:81]
	s_movk_i32 s7, 0x2900
	s_ashr_i32 s5, s4, 31
	v_ashrrev_i32_e32 v203, 31, v202
	v_mad_i64_i32 v[198:199], s[12:13], v196, s7, v[160:161]
	s_lshl_b32 s96, s9, 8
	s_lshl_b64 s[4:5], s[4:5], 12
	s_lshl_b32 s1, s1, 7
	s_waitcnt lgkmcnt(0)
	v_lshl_add_u64 v[0:1], v[198:199], 0, s[96:97]
	v_lshlrev_b64 v[176:177], 1, v[202:203]
	s_or_b32 s1, s4, s1
	v_lshl_add_u64 v[8:9], v[0:1], 0, v[176:177]
	v_mov_b32_e32 v0, s1
	v_mov_b32_e32 v1, s5
	v_readlane_b32 s4, v253, 46
	v_lshlrev_b64 v[0:1], 8, v[0:1]
	v_readlane_b32 s5, v253, 47
	v_or_b32_e32 v194, 16, v196
	s_movk_i32 s6, 0x1000
	v_lshl_add_u64 v[0:1], s[4:5], 0, v[0:1]
	v_mad_i64_i32 v[200:201], s[4:5], v194, s7, v[160:161]
	v_add_co_u32_e32 v4, vcc, s6, v8
	s_mov_b64 s[4:5], 0x1000
	v_lshlrev_b32_e32 v2, 4, v180
	v_lshl_or_b32 v2, v205, 8, v2
	v_mov_b32_e32 v3, 0
	v_lshl_add_u64 v[36:37], v[0:1], 0, v[2:3]
	v_addc_co_u32_e32 v5, vcc, 0, v9, vcc
	v_lshl_add_u64 v[8:9], v[8:9], 0, s[4:5]
	global_load_dwordx4 v[0:3], v[36:37], off
	global_load_dwordx4 v[46:49], v[36:37], off offset:1024
	v_and_b32_e32 v242, -16, v196
	v_lshlrev_b32_e32 v242, 12, v242
	v_lshl_add_u32 v242, v180, 4, v242
	v_lshl_add_u32 v242, v205, 8, v242
	s_lshl_b32 s100, s9, 12
	v_add_u32_e32 v242, s100, v242
	v_add_u32_e32 v242, 0xe000000, v242
	v_mov_b32_e32 v243, 0
	v_mov_b32_e32 v238, s62
	v_mov_b32_e32 v239, s63
	v_lshl_add_u64 v[238:239], v[238:239], 0, v[242:243]
	v_mov_b32_e32 v242, 0x10000
	v_lshl_add_u64 v[240:241], v[238:239], 0, v[242:243]
	v_and_b32_e32 v242, -16, v196
	v_lshlrev_b32_e32 v242, 11, v242
	v_lshl_add_u32 v242, v180, 4, v242
	v_lshrrev_b32_e32 v243, 1, v205
	v_lshl_add_u32 v242, v243, 8, v242
	v_and_b32_e32 v243, 1, v205
	v_lshl_add_u32 v242, v243, 3, v242
	v_add_u32_e32 v242, s100, v242
	v_add_u32_e32 v242, 0x2ec00000, v242
	v_mov_b32_e32 v243, 0
	v_mov_b32_e32 v248, s62
	v_mov_b32_e32 v249, s63
	v_lshl_add_u64 v[248:249], v[248:249], 0, v[242:243]
	global_load_dwordx4 v[20:23], v[238:239], off
	global_load_dwordx4 v[52:55], v[238:239], off offset:1024
	v_lshl_add_u64 v[4:5], v[200:201], 0, s[96:97]
	v_lshl_add_u64 v[12:13], v[4:5], 0, v[176:177]
	v_add_co_u32_e32 v4, vcc, s6, v12
	v_lshl_add_u64 v[80:81], v[12:13], 0, s[4:5]
	s_nop 0
	v_addc_co_u32_e32 v5, vcc, 0, v13, vcc
	global_load_dwordx4 v[24:27], v[240:241], off
	global_load_dwordx4 v[60:63], v[238:239], off offset:2048
	global_load_dwordx4 v[56:59], v[240:241], off offset:1024
	global_load_dwordx4 v[64:67], v[240:241], off offset:2048
	s_movk_i32 s1, 0x2000
	v_add_co_u32_e32 v10, vcc, s1, v36
	s_movk_i32 s1, 0x4000
	s_nop 0
	v_addc_co_u32_e32 v11, vcc, 0, v37, vcc
	s_waitcnt lgkmcnt(0)
	global_load_dwordx4 v[14:17], v[10:11], off offset:-4096
	global_load_dwordx4 v[72:75], v[238:239], off offset:3072
	s_waitcnt vmcnt(19)
	v_add_co_u32_e32 v50, vcc, s1, v36
	global_load_dwordx4 v[28:31], v[10:11], off
	s_nop 0
	v_addc_co_u32_e32 v51, vcc, 0, v37, vcc
	v_add_co_u32_e32 v84, vcc, s6, v36
	global_load_dwordx4 v[38:41], v[50:51], off offset:-4096
	global_load_dwordx4 v[112:115], v[50:51], off offset:2048
	v_addc_co_u32_e32 v85, vcc, 0, v37, vcc
	s_movk_i32 s1, 0x3000
	v_lshlrev_b32_e32 v119, 1, v118
	v_and_b32_e32 v118, 3, v118
	s_mov_b64 s[10:11], 0x1800
	s_lshl_b32 s9, s9, 7
	v_or_b32_e32 v228, 16, v209
	v_mov_b32_e32 v210, v202
	v_mov_b32_e32 v195, v202
	s_waitcnt vmcnt(10)
	v_mfma_f32_16x16x32_bf16 v[4:7], v[0:3], v[20:23], 0
	global_load_dwordx4 v[80:83], v[240:241], off offset:3072
	s_waitcnt vmcnt(9)
	v_mfma_f32_16x16x32_bf16 v[0:3], v[0:3], v[24:27], 0
	v_mfma_f32_16x16x32_bf16 v[4:7], v[46:49], v[52:55], v[4:7]
	s_waitcnt vmcnt(7)
	v_mfma_f32_16x16x32_bf16 v[0:3], v[46:49], v[56:59], v[0:3]
	global_load_dwordx4 v[46:49], v[84:85], off offset:1024
	s_waitcnt vmcnt(6)
	v_mfma_f32_16x16x32_bf16 v[32:35], v[14:17], v[20:23], 0
	v_mfma_f32_16x16x32_bf16 v[14:17], v[14:17], v[24:27], 0
	s_waitcnt vmcnt(3)
	v_mfma_f32_16x16x32_bf16 v[68:71], v[38:41], v[20:23], 0
	s_waitcnt vmcnt(0)
	v_mfma_f32_16x16x32_bf16 v[12:15], v[46:49], v[56:59], v[14:17]
	s_nop 3
	global_load_dwordx4 v[16:19], v[10:11], off offset:1024
	v_mfma_f32_16x16x32_bf16 v[42:45], v[28:31], v[20:23], 0
	v_mfma_f32_16x16x32_bf16 v[28:31], v[28:31], v[24:27], 0
	v_mfma_f32_16x16x32_bf16 v[32:35], v[46:49], v[52:55], v[32:35]
	global_load_dwordx4 v[46:49], v[36:37], off offset:2048
	s_waitcnt vmcnt(1)
	v_mfma_f32_16x16x32_bf16 v[42:45], v[16:19], v[52:55], v[42:45]
	v_mfma_f32_16x16x32_bf16 v[16:19], v[16:19], v[56:59], v[28:31]
	s_nop 2
	global_load_dwordx4 v[28:31], v[84:85], off offset:2048
	s_waitcnt vmcnt(0)
	v_mfma_f32_16x16x32_bf16 v[76:79], v[28:31], v[64:67], v[12:15]
	s_nop 2
	global_load_dwordx4 v[12:15], v[36:37], off offset:3072
	v_mfma_f32_16x16x32_bf16 v[4:7], v[46:49], v[60:63], v[4:7]
	v_mfma_f32_16x16x32_bf16 v[0:3], v[46:49], v[64:67], v[0:3]
	v_mfma_f32_16x16x32_bf16 v[46:49], v[28:31], v[60:63], v[32:35]
	s_nop 2
	global_load_dwordx4 v[32:35], v[10:11], off offset:2048
	s_waitcnt vmcnt(1)
	v_mfma_f32_16x16x32_bf16 v[28:31], v[12:15], v[80:83], v[0:3]
	s_nop 2
	global_load_dwordx4 v[0:3], v[10:11], off offset:3072
	s_waitcnt vmcnt(1)
; __device__ __forceinline__ f32x4 mfma16(bf16x8 a, bf16x8 b, f32x4 c) { return __builtin_amdgcn_mfma_f32_16x16x32_bf16(a, b, c, 0, 0, 0); }
; __device__ __forceinline__ void ret_task(const Frame& F, int l, int task) {
;     ...
;     bf16x8 Qf[2][4], Kf[2][2][4];
; #pragma unroll
;     for (int qb = 0; qb < 2; ++qb)
; #pragma unroll
;         for (int ks = 0; ks < 4; ++ks) Qf[qb][ks] = ld_b8(TOK + (size_t)(tq0 + qb * 16 + c) * TOKP + TK_QR + h * HD + ks * 32 + rq * 8);
; #pragma unroll
;     for (int g = 0; g < 2; ++g)
; #pragma unroll
;         for (int ab = 0; ab < 2; ++ab) { const int key = 32 * g + (c >> 2) * 8 + 4 * ab + (c & 3);
; #pragma unroll
;             for (int ks = 0; ks < 4; ++ks) Kf[g][ab][ks] = ld_b8(TOK + (size_t)(tc0 + key) * TOKP + TK_KR + h * HD + rq * 8 + ks * 32); }
;     f32x4 acc[2][8];
; #pragma unroll
;     for (int qb = 0; qb < 2; ++qb)
; #pragma unroll
;         for (int eb = 0; eb < 8; ++eb) acc[qb][eb] = (f32x4){0.f, 0.f, 0.f, 0.f};
;     const bf16* sp = ST + (((size_t)bhh * NCH + n) * HD + c) * HD + rq * 8;
; #pragma unroll
;     for (int eb = 0; eb < 8; ++eb)
; #pragma unroll
;         for (int ks = 0; ks < 4; ++ks) { const bf16x8 sf = ld_b8(sp + eb * 16 * HD + ks * 32);
; #pragma unroll
;             for (int qb = 0; qb < 2; ++qb) acc[qb][eb] = mfma16(sf, Qf[qb][ks], acc[qb][eb]); }
;     bf16x8 Vf[8];
; #pragma unroll
;     for (int eb = 0; eb < 8; ++eb) Vf[eb] = ld_b8(SWP + (size_t)(SW_VR + h * HD + eb * 16 + c) * SWPP + tc0 + 8 * rq);
	v_mfma_f32_16x16x32_bf16 v[42:45], v[32:35], v[60:63], v[42:45]
	v_mfma_f32_16x16x32_bf16 v[16:19], v[32:35], v[64:67], v[16:19]
	v_mfma_f32_16x16x32_bf16 v[32:35], v[12:15], v[72:75], v[4:7]
	s_nop 2
	global_load_dwordx4 v[4:7], v[84:85], off offset:3072
	v_add_co_u32_e32 v84, vcc, s1, v36
	s_movk_i32 s1, 0x6000
	s_nop 0
	v_addc_co_u32_e32 v85, vcc, 0, v37, vcc
	s_waitcnt vmcnt(0)
	v_mfma_f32_16x16x32_bf16 v[12:15], v[4:7], v[72:75], v[46:49]
	s_nop 2
	global_load_dwordx4 v[46:49], v[84:85], off offset:1024
	v_add_co_u32_e32 v116, vcc, s1, v36
	v_mfma_f32_16x16x32_bf16 v[8:11], v[4:7], v[80:83], v[76:79]
	s_nop 0
	v_addc_co_u32_e32 v117, vcc, 0, v37, vcc
	s_movk_i32 s1, 0x5000
	v_mfma_f32_16x16x32_bf16 v[4:7], v[0:3], v[72:75], v[42:45]
	global_load_dwordx4 v[76:79], v[84:85], off offset:3072
	global_load_dwordx4 v[92:95], v[116:117], off
	global_load_dwordx4 v[88:91], v[116:117], off offset:1024
	global_load_dwordx4 v[42:45], v[84:85], off offset:2048
	v_mfma_f32_16x16x32_bf16 v[0:3], v[0:3], v[80:83], v[16:19]
	global_load_dwordx4 v[108:111], v[116:117], off offset:-4096
	v_mfma_f32_16x16x32_bf16 v[16:19], v[38:41], v[24:27], 0
	s_waitcnt vmcnt(5)
	v_mfma_f32_16x16x32_bf16 v[38:41], v[46:49], v[52:55], v[68:71]
	s_nop 2
	global_load_dwordx4 v[68:71], v[50:51], off offset:1024
	global_load_dwordx4 v[84:87], v[50:51], off
	v_mfma_f32_16x16x32_bf16 v[16:19], v[46:49], v[56:59], v[16:19]
	s_waitcnt vmcnt(3)
	v_mfma_f32_16x16x32_bf16 v[38:41], v[42:45], v[60:63], v[38:41]
	v_mfma_f32_16x16x32_bf16 v[42:45], v[42:45], v[64:67], v[16:19]
	v_mfma_f32_16x16x32_bf16 v[16:19], v[76:79], v[72:75], v[38:41]
	s_nop 5
	v_add_co_u32_e32 v38, vcc, s1, v36
	v_mfma_f32_16x16x32_bf16 v[40:43], v[76:79], v[80:83], v[42:45]
	s_nop 0
	v_addc_co_u32_e32 v39, vcc, 0, v37, vcc
	global_load_dwordx4 v[96:99], v[38:39], off offset:3072
	global_load_dwordx4 v[104:107], v[38:39], off offset:1024
	global_load_dwordx4 v[100:103], v[38:39], off offset:2048
	s_waitcnt vmcnt(3)
	v_mfma_f32_16x16x32_bf16 v[44:47], v[84:87], v[20:23], 0
	global_load_dwordx4 v[48:51], v[50:51], off offset:3072
	s_movk_i32 s1, 0x7000
	v_mfma_f32_16x16x32_bf16 v[76:79], v[84:87], v[24:27], 0
	v_mfma_f32_16x16x32_bf16 v[44:47], v[68:71], v[52:55], v[44:47]
	v_mfma_f32_16x16x32_bf16 v[68:71], v[68:71], v[56:59], v[76:79]
	s_nop 5
	global_load_dwordx4 v[76:79], v[116:117], off offset:2048
	global_load_dwordx4 v[84:87], v[116:117], off offset:3072
	v_add_co_u32_e32 v116, vcc, s1, v36
	v_mfma_f32_16x16x32_bf16 v[44:47], v[112:115], v[60:63], v[44:47]
	s_nop 0
	v_addc_co_u32_e32 v117, vcc, 0, v37, vcc
	global_load_dwordx4 v[36:39], v[116:117], off offset:1024
	v_mfma_f32_16x16x32_bf16 v[112:115], v[112:115], v[64:67], v[68:71]
	s_ashr_i32 s1, s0, 31
	s_nop 1
	global_load_dwordx4 v[68:71], v[116:117], off
	s_waitcnt vmcnt(4)
	v_mfma_f32_16x16x32_bf16 v[44:47], v[48:51], v[72:75], v[44:47]
	v_mfma_f32_16x16x32_bf16 v[48:51], v[48:51], v[80:83], v[112:115]
	s_nop 2
	v_and_b32_e32 v112, 24, v119
	v_mfma_f32_16x16x32_bf16 v[120:123], v[108:111], v[20:23], 0
	v_or3_b32 v162, v118, v112, s0
	v_and_b32_e32 v242, -16, v162
	v_lshlrev_b32_e32 v242, 12, v242
	v_and_b32_e32 v243, 15, v162
	v_lshl_add_u32 v242, v243, 4, v242
	v_lshl_add_u32 v242, v205, 8, v242
	s_lshl_b32 s100, s9, 5
	s_add_i32 s100, s100, 0x8000
	v_add_u32_e32 v242, s100, v242
	v_add_u32_e32 v242, 0xe000000, v242
	v_mov_b32_e32 v243, 0
	v_mov_b32_e32 v244, s62
	v_mov_b32_e32 v245, s63
	v_lshl_add_u64 v[244:245], v[244:245], 0, v[242:243]
	v_mov_b32_e32 v242, 0x20000
	v_lshl_add_u64 v[246:247], v[244:245], 0, v[242:243]
	v_mad_i64_i32 v[118:119], s[4:5], v162, s7, v[160:161]
	v_mfma_f32_16x16x32_bf16 v[124:127], v[108:111], v[24:27], 0
	global_load_dwordx4 v[112:115], v[116:117], off offset:2048
	v_lshl_add_u64 v[118:119], v[118:119], 0, s[96:97]
	v_lshl_add_u64 v[128:129], v[118:119], 0, v[176:177]
	v_mfma_f32_16x16x32_bf16 v[120:123], v[104:107], v[52:55], v[120:123]
	v_add_co_u32_e32 v108, vcc, s6, v128
	v_mfma_f32_16x16x32_bf16 v[104:107], v[104:107], v[56:59], v[124:127]
	s_nop 0
	v_addc_co_u32_e32 v109, vcc, 0, v129, vcc
	v_lshl_add_u64 v[128:129], v[128:129], 0, s[10:11]
	v_or_b32_e32 v124, 4, v162
	v_mad_i64_i32 v[124:125], s[4:5], v124, s7, v[160:161]
	v_lshl_add_u64 v[124:125], v[124:125], 0, s[96:97]
	global_load_dwordx4 v[108:111], v[244:245], off
	v_lshl_add_u64 v[130:131], v[124:125], 0, v[176:177]
	global_load_dwordx4 v[124:127], v[244:245], off offset:1024
	v_mfma_f32_16x16x32_bf16 v[120:123], v[100:103], v[60:63], v[120:123]
	global_load_dwordx4 v[116:119], v[116:117], off offset:3072
	v_mfma_f32_16x16x32_bf16 v[100:103], v[100:103], v[64:67], v[104:107]
	s_nop 2
	v_add_co_u32_e32 v104, vcc, s6, v130
	v_mfma_f32_16x16x32_bf16 v[144:147], v[96:99], v[72:75], v[120:123]
	s_nop 0
	v_addc_co_u32_e32 v105, vcc, 0, v131, vcc
	v_or_b32_e32 v106, s9, v180
	global_load_dwordx4 v[120:123], v[244:245], off offset:64
	v_mfma_f32_16x16x32_bf16 v[148:151], v[96:99], v[80:83], v[100:103]
	global_load_dwordx4 v[168:171], v[244:245], off offset:2048
	global_load_dwordx4 v[96:99], v[244:245], off offset:3072
	v_mul_u32_u24_e32 v106, 0x4080, v106
	v_lshlrev_b32_e32 v184, 1, v106
	v_mfma_f32_16x16x32_bf16 v[100:103], v[92:95], v[20:23], 0
	v_or_b32_e32 v104, 32, v162
	v_lshl_add_u64 v[106:107], s[64:65], 0, v[184:185]
	v_mad_i64_i32 v[104:105], s[4:5], v104, s7, v[160:161]
	v_mfma_f32_16x16x32_bf16 v[92:95], v[92:95], v[24:27], 0
	v_lshl_add_u64 v[106:107], s[0:1], 1, v[106:107]
	v_lshl_add_u64 v[178:179], v[106:107], 0, v[176:177]
	v_lshlrev_b32_e32 v242, 4, v180
	v_lshl_add_u32 v242, v205, 8, v242
	v_lshl_add_u32 v242, s9, 15, v242
	v_lshl_add_u32 v242, s0, 5, v242
	v_add_u32_e32 v242, 0x30c00000, v242
	v_mov_b32_e32 v243, 0
	v_mov_b32_e32 v238, s62
	v_mov_b32_e32 v239, s63
	v_lshl_add_u64 v[238:239], v[238:239], 0, v[242:243]
	v_mov_b32_e32 v178, v238
	v_mov_b32_e32 v179, v239
	s_mov_b32 s4, 0x380000
	v_mfma_f32_16x16x32_bf16 v[100:103], v[88:91], v[52:55], v[100:103]
	v_add_co_u32_e32 v106, vcc, s4, v178
	v_lshl_add_u64 v[128:129], v[130:131], 0, s[10:11]
	v_mfma_f32_16x16x32_bf16 v[88:91], v[88:91], v[56:59], v[92:95]
	v_addc_co_u32_e32 v107, vcc, 0, v179, vcc
	s_waitcnt vmcnt(10)
; __device__ __forceinline__ f32x4 mfma16(bf16x8 a, bf16x8 b, f32x4 c) { return __builtin_amdgcn_mfma_f32_16x16x32_bf16(a, b, c, 0, 0, 0); }
; __device__ __forceinline__ float fexp2(float x) { return __builtin_amdgcn_exp2f(x); }
; __device__ __forceinline__ void ret_task(const Frame& F, int l, int task) {
;     ...
; #pragma unroll
;     for (int eb = 0; eb < 8; ++eb)
; #pragma unroll
;         for (int ks = 0; ks < 4; ++ks) { const bf16x8 sf = ld_b8(sp + eb * 16 * HD + ks * 32);
; #pragma unroll
;             for (int qb = 0; qb < 2; ++qb) acc[qb][eb] = mfma16(sf, Qf[qb][ks], acc[qb][eb]); }
;     bf16x8 Vf[8];
; #pragma unroll
;     for (int eb = 0; eb < 8; ++eb) Vf[eb] = ld_b8(SWP + (size_t)(SW_VR + h * HD + eb * 16 + c) * SWPP + tc0 + 8 * rq);
; #pragma unroll
;     for (int qb = 0; qb < 2; ++qb) { const float f = fexp2((float)(qb2 * 32 + qb * 16 + c + 1) * lg);
; #pragma unroll
;         for (int eb = 0; eb < 8; ++eb) acc[qb][eb] *= f; }
;     f32x4 g4[8]; u32x2 gwq[2][8];
; #pragma unroll
;     for (int g = 0; g < 2; ++g) {
;         if (g <= qb2) {
;             f32x4 sa[2][2];
; #pragma unroll
;             for (int qb = 0; qb < 2; ++qb)
; #pragma unroll
;                 for (int ab = 0; ab < 2; ++ab) sa[qb][ab] = (f32x4){0.f, 0.f, 0.f, 0.f};
; #pragma unroll
;             for (int ab = 0; ab < 2; ++ab)
; #pragma unroll
;                 for (int ks = 0; ks < 4; ++ks)
; #pragma unroll
;                     for (int qb = 0; qb < 2; ++qb) sa[qb][ab] = mfma16(Kf[g][ab][ks], Qf[qb][ks], sa[qb][ab]);
;             bf16x8 Pf[2];
; #pragma unroll
;             for (int qb = 0; qb < 2; ++qb) {
;                 const int i = qb2 * 32 + qb * 16 + c;
; #pragma unroll
;                 for (int ab = 0; ab < 2; ++ab)
; #pragma unroll
;                     for (int e = 0; e < 4; ++e) { const int diff = i - (32 * g + 8 * rq + 4 * ab + e);
;                         sa[qb][ab][e] = diff >= 0 ? sa[qb][ab][e] * fexp2((float)diff * lg) : 0.f; }
	v_mfma_f32_16x16x32_bf16 v[92:95], v[76:79], v[60:63], v[100:103]
	v_mfma_f32_16x16x32_bf16 v[100:103], v[76:79], v[64:67], v[88:91]
	global_load_dwordx4 v[76:79], v[106:107], off
	global_load_dwordx4 v[172:175], v[244:245], off offset:1088
	s_nop 1
	v_lshl_add_u64 v[88:89], v[104:105], 0, s[96:97]
	s_waitcnt vmcnt(11)
	v_mfma_f32_16x16x32_bf16 v[152:155], v[84:87], v[72:75], v[92:95]
	v_lshl_add_u64 v[104:105], v[88:89], 0, v[176:177]
	global_load_dwordx4 v[88:91], v[244:245], off offset:3136
	v_lshl_add_u64 v[106:107], v[104:105], 0, s[10:11]
	v_mfma_f32_16x16x32_bf16 v[156:159], v[84:87], v[80:83], v[100:103]
	global_load_dwordx4 v[84:87], v[244:245], off offset:2112
	v_add_co_u32_e32 v104, vcc, s6, v104
	s_waitcnt vmcnt(11)
	v_mfma_f32_16x16x32_bf16 v[92:95], v[68:71], v[20:23], 0
	v_addc_co_u32_e32 v105, vcc, 0, v105, vcc
	global_load_dwordx4 v[132:135], v[246:247], off offset:1024
	global_load_dwordx4 v[128:131], v[246:247], off offset:2048
	v_mfma_f32_16x16x32_bf16 v[100:103], v[68:71], v[24:27], 0
	v_or_b32_e32 v68, 36, v162
	v_mad_i64_i32 v[68:69], s[4:5], v68, s7, v[160:161]
	v_mfma_f32_16x16x32_bf16 v[92:95], v[36:39], v[52:55], v[92:95]
	s_mov_b32 s4, 0
	v_add_co_u32_e32 v70, vcc, s4, v178
	v_mfma_f32_16x16x32_bf16 v[36:39], v[36:39], v[56:59], v[100:103]
	s_nop 0
	v_addc_co_u32_e32 v71, vcc, 0, v179, vcc
	s_mov_b32 s4, 0x80000
	s_waitcnt vmcnt(12)
	v_mfma_f32_16x16x32_bf16 v[36:39], v[112:115], v[64:67], v[36:39]
	global_load_dwordx4 v[140:143], v[246:247], off
	global_load_dwordx4 v[136:139], v[246:247], off offset:3072
	v_lshl_add_u64 v[68:69], v[68:69], 0, s[96:97]
	v_lshl_add_u64 v[68:69], v[68:69], 0, v[176:177]
	v_mfma_f32_16x16x32_bf16 v[100:103], v[112:115], v[60:63], v[92:95]
	s_nop 2
	global_load_dwordx4 v[92:95], v[70:71], off
	v_add_co_u32_e32 v70, vcc, s4, v178
	s_mov_b32 s4, 0x100000
	s_nop 0
	v_addc_co_u32_e32 v71, vcc, 0, v179, vcc
	v_add_co_u32_e32 v104, vcc, s4, v178
	s_waitcnt vmcnt(12)
	v_mfma_f32_16x16x32_bf16 v[164:167], v[116:119], v[80:83], v[36:39]
	v_addc_co_u32_e32 v105, vcc, 0, v179, vcc
	s_mov_b32 s4, 0x180000
	v_mfma_f32_16x16x32_bf16 v[36:39], v[108:111], v[20:23], 0
	v_mfma_f32_16x16x32_bf16 v[108:111], v[108:111], v[24:27], 0
	v_mfma_f32_16x16x32_bf16 v[160:163], v[116:119], v[72:75], v[100:103]
	s_nop 2
	global_load_dwordx4 v[100:103], v[70:71], off
	s_nop 0
	global_load_dwordx4 v[104:107], v[104:105], off
	v_add_co_u32_e32 v70, vcc, s4, v178
	s_mov_b32 s4, 0x200000
	s_nop 0
	v_addc_co_u32_e32 v71, vcc, 0, v179, vcc
	v_add_co_u32_e32 v116, vcc, s4, v178
	v_readlane_b32 s4, v251, 33
	s_nop 0
	v_addc_co_u32_e32 v117, vcc, 0, v179, vcc
	v_mfma_f32_16x16x32_bf16 v[36:39], v[124:127], v[52:55], v[36:39]
	global_load_dwordx4 v[112:115], v[70:71], off
	s_nop 0
	global_load_dwordx4 v[116:119], v[116:117], off
	v_add_u32_e32 v70, s4, v180
	v_cvt_f32_ubyte0_e32 v71, v70
	v_mfma_f32_16x16x32_bf16 v[108:111], v[124:127], v[56:59], v[108:111]
	v_add_u32_e32 v70, 16, v70
	v_cvt_f32_ubyte0_e32 v70, v70
	v_or_b32_e32 v126, 2, v202
	v_mul_f32_e32 v71, v197, v71
	v_mul_f32_e32 v70, v197, v70
	s_waitcnt vmcnt(14)
	v_mfma_f32_16x16x32_bf16 v[36:39], v[168:171], v[60:63], v[36:39]
	v_exp_f32_e32 v204, v71
	v_exp_f32_e32 v206, v70
	v_or_b32_e32 v127, 3, v202
	v_mfma_f32_16x16x32_bf16 v[108:111], v[168:171], v[64:67], v[108:111]
	v_sub_u32_e32 v169, v209, v202
	v_sub_u32_e32 v170, v209, v126
	v_cvt_f32_u32_e32 v70, v169
	v_cvt_f32_u32_e32 v71, v170
	s_waitcnt vmcnt(13)
	v_mfma_f32_16x16x32_bf16 v[36:39], v[96:99], v[72:75], v[36:39]
	v_or_b32_e32 v168, 1, v202
	v_mul_f32_e32 v70, v197, v70
	v_mul_f32_e32 v71, v197, v71
	v_exp_f32_e32 v70, v70
	v_exp_f32_e32 v71, v71
	v_mfma_f32_16x16x32_bf16 v[96:99], v[96:99], v[80:83], v[108:111]
	s_nop 1
	v_mov_b32_e32 v124, v36
	v_mov_b32_e32 v125, v38
	v_pk_mul_f32 v[70:71], v[70:71], v[124:125]
	v_mfma_f32_16x16x32_bf16 v[108:111], v[120:123], v[20:23], 0
	v_cmp_lt_i32_e32 vcc, -1, v170
	v_sub_u32_e32 v125, v209, v127
	v_cvt_f32_u32_e32 v38, v125
	v_mfma_f32_16x16x32_bf16 v[120:123], v[120:123], v[24:27], 0
	v_cndmask_b32_e32 v124, 0, v71, vcc
	v_sub_u32_e32 v71, v209, v168
	v_cvt_f32_u32_e32 v36, v71
	s_waitcnt vmcnt(11)
	v_mfma_f32_16x16x32_bf16 v[108:111], v[172:175], v[52:55], v[108:111]
	v_cmp_lt_i32_e32 vcc, -1, v169
	v_pk_mul_f32 v[14:15], v[204:205], v[14:15] op_sel_hi:[0,1]
	v_mul_f32_e32 v36, v197, v36
	v_mfma_f32_16x16x32_bf16 v[120:123], v[172:175], v[56:59], v[120:123]
	v_mul_f32_e64 v12, v204, v12
	v_mul_f32_e64 v13, v204, v13
	s_mov_b32 s4, 0x280000
	v_pk_mul_f32 v[6:7], v[204:205], v[6:7] op_sel_hi:[0,1]
	s_waitcnt vmcnt(9)
; __device__ __forceinline__ f32x4 mfma16(bf16x8 a, bf16x8 b, f32x4 c) { return __builtin_amdgcn_mfma_f32_16x16x32_bf16(a, b, c, 0, 0, 0); }
; __device__ __forceinline__ float fexp2(float x) { return __builtin_amdgcn_exp2f(x); }
; __device__ __forceinline__ void ret_task(const Frame& F, int l, int task) {
;     ...
;     for (int eb = 0; eb < 8; ++eb) Vf[eb] = ld_b8(SWP + (size_t)(SW_VR + h * HD + eb * 16 + c) * SWPP + tc0 + 8 * rq);
; #pragma unroll
;     for (int qb = 0; qb < 2; ++qb) { const float f = fexp2((float)(qb2 * 32 + qb * 16 + c + 1) * lg);
; #pragma unroll
;         for (int eb = 0; eb < 8; ++eb) acc[qb][eb] *= f; }
;     f32x4 g4[8]; u32x2 gwq[2][8];
; #pragma unroll
;     for (int g = 0; g < 2; ++g) {
;         if (g <= qb2) {
;             f32x4 sa[2][2];
; #pragma unroll
;             for (int qb = 0; qb < 2; ++qb)
; #pragma unroll
;                 for (int ab = 0; ab < 2; ++ab) sa[qb][ab] = (f32x4){0.f, 0.f, 0.f, 0.f};
; #pragma unroll
;             for (int ab = 0; ab < 2; ++ab)
; #pragma unroll
;                 for (int ks = 0; ks < 4; ++ks)
; #pragma unroll
;                     for (int qb = 0; qb < 2; ++qb) sa[qb][ab] = mfma16(Kf[g][ab][ks], Qf[qb][ks], sa[qb][ab]);
;             bf16x8 Pf[2];
; #pragma unroll
;             for (int qb = 0; qb < 2; ++qb) {
;                 const int i = qb2 * 32 + qb * 16 + c;
; #pragma unroll
;                 for (int ab = 0; ab < 2; ++ab)
; #pragma unroll
;                     for (int e = 0; e < 4; ++e) { const int diff = i - (32 * g + 8 * rq + 4 * ab + e);
;                         sa[qb][ab][e] = diff >= 0 ? sa[qb][ab][e] * fexp2((float)diff * lg) : 0.f; }
;                 Pf[qb] = pack8(sa[qb][0], sa[qb][1]);
;             }
; #pragma unroll
;             for (int eb = 0; eb < 8; ++eb)
; #pragma unroll
;                 for (int qb = 0; qb < 2; ++qb) acc[qb][eb] = mfma16(Vf[eb], Pf[qb], acc[qb][eb]);
	v_mfma_f32_16x16x32_bf16 v[108:111], v[84:87], v[60:63], v[108:111]
	v_mul_f32_e64 v4, v204, v4
	v_mul_f32_e64 v5, v204, v5
	v_pk_mul_f32 v[30:31], v[206:207], v[30:31] op_sel_hi:[0,1]
	v_pk_mul_f32 v[28:29], v[206:207], v[28:29] op_sel_hi:[0,1]
	v_mfma_f32_16x16x32_bf16 v[84:87], v[84:87], v[64:67], v[120:123]
	v_mul_f32_e64 v2, v206, v2
	v_mul_f32_e64 v3, v206, v3
	v_pk_mul_f32 v[0:1], v[206:207], v[0:1] op_sel_hi:[0,1]
	v_pk_mul_f32 v[34:35], v[204:205], v[34:35] op_sel_hi:[0,1]
	v_exp_f32_e32 v120, v36
	v_mul_f32_e32 v36, v197, v38
	v_exp_f32_e32 v121, v36
	v_mov_b32_e32 v38, v37
	v_cndmask_b32_e32 v122, 0, v70, vcc
	v_cmp_lt_i32_e32 vcc, -1, v71
	v_pk_mul_f32 v[36:37], v[120:121], v[38:39]
	v_mfma_f32_16x16x32_bf16 v[108:111], v[88:91], v[72:75], v[108:111]
	v_sub_u32_e32 v39, v228, v126
	v_cvt_f32_u32_e32 v70, v39
	v_sub_u32_e32 v120, v228, v127
	v_mfma_f32_16x16x32_bf16 v[84:87], v[88:91], v[80:83], v[84:87]
	v_cndmask_b32_e32 v88, 0, v36, vcc
	v_cmp_lt_i32_e32 vcc, -1, v125
	v_sub_u32_e32 v91, v228, v168
	v_sub_u32_e32 v89, v228, v202
	v_cndmask_b32_e32 v90, 0, v37, vcc
	v_cvt_f32_u32_e32 v37, v91
	v_cvt_f32_u32_e32 v36, v89
	v_mov_b32_e32 v71, v98
	v_cmp_lt_i32_e32 vcc, -1, v39
	v_mul_f32_e32 v37, v197, v37
	v_mul_f32_e32 v36, v197, v36
	v_exp_f32_e32 v38, v37
	v_mul_f32_e32 v37, v197, v70
	v_exp_f32_e32 v36, v36
	v_exp_f32_e32 v37, v37
	v_mov_b32_e32 v70, v96
	v_cvt_f32_u32_e32 v96, v120
	v_mov_b32_e32 v98, v97
	v_pk_mul_f32 v[36:37], v[36:37], v[70:71]
	v_or_b32_e32 v123, 5, v202
	v_cndmask_b32_e32 v121, 0, v37, vcc
	v_mul_f32_e32 v37, v197, v96
	v_exp_f32_e32 v39, v37
	v_cmp_lt_i32_e32 vcc, -1, v89
	v_or_b32_e32 v97, 6, v202
	v_sub_u32_e32 v125, v209, v123
	v_cndmask_b32_e32 v89, 0, v36, vcc
	v_pk_mul_f32 v[36:37], v[38:39], v[98:99]
	v_cmp_lt_i32_e32 vcc, -1, v91
	v_or_b32_e32 v98, 4, v202
	v_sub_u32_e32 v99, v209, v98
	v_cndmask_b32_e32 v91, 0, v36, vcc
	v_cmp_lt_i32_e32 vcc, -1, v120
	v_sub_u32_e32 v39, v209, v97
	v_cvt_f32_u32_e32 v36, v99
	v_cndmask_b32_e32 v96, 0, v37, vcc
	v_cvt_f32_u32_e32 v37, v125
	v_cvt_f32_u32_e32 v70, v39
	v_or_b32_e32 v120, 7, v202
	v_mul_f32_e32 v36, v197, v36
	v_mul_f32_e32 v37, v197, v37
	v_exp_f32_e32 v38, v37
	v_mul_f32_e32 v37, v197, v70
	v_exp_f32_e32 v36, v36
	v_sub_u32_e32 v126, v209, v120
	v_exp_f32_e32 v37, v37
	v_mov_b32_e32 v70, v108
	v_cvt_f32_u32_e32 v108, v126
	v_mov_b32_e32 v71, v110
	v_pk_mul_f32 v[36:37], v[36:37], v[70:71]
	v_cmp_lt_i32_e32 vcc, -1, v39
	v_mov_b32_e32 v110, v109
	v_sub_u32_e32 v98, v228, v98
	v_cndmask_b32_e32 v127, 0, v37, vcc
	v_mul_f32_e32 v37, v197, v108
	v_exp_f32_e32 v39, v37
	v_cmp_lt_i32_e32 vcc, -1, v99
	v_mov_b32_e32 v71, v86
	v_mov_b32_e32 v86, v85
	v_cndmask_b32_e32 v99, 0, v36, vcc
	v_pk_mul_f32 v[36:37], v[38:39], v[110:111]
	v_cmp_lt_i32_e32 vcc, -1, v125
	v_sub_u32_e32 v39, v228, v97
	v_sub_u32_e32 v97, v228, v123
	v_cndmask_b32_e32 v108, 0, v36, vcc
	v_cmp_lt_i32_e32 vcc, -1, v126
	v_cvt_f32_u32_e32 v36, v98
	v_cvt_f32_u32_e32 v70, v39
	v_cndmask_b32_e32 v109, 0, v37, vcc
	v_cvt_f32_u32_e32 v37, v97
	v_mul_f32_e32 v36, v197, v36
	v_exp_f32_e32 v36, v36
	v_sub_u32_e32 v110, v228, v120
	v_mul_f32_e32 v37, v197, v37
	v_exp_f32_e32 v38, v37
	v_mul_f32_e32 v37, v197, v70
	v_exp_f32_e32 v37, v37
	v_mov_b32_e32 v70, v84
	v_cvt_f32_u32_e32 v84, v110
	v_cmp_lt_i32_e32 vcc, -1, v39
	v_pk_mul_f32 v[36:37], v[36:37], v[70:71]
	s_nop 0
	v_cndmask_b32_e32 v70, 0, v37, vcc
	v_mul_f32_e32 v37, v197, v84
	v_exp_f32_e32 v39, v37
	v_cmp_lt_i32_e32 vcc, -1, v98
	s_nop 1
	v_cndmask_b32_e32 v71, 0, v36, vcc
	v_pk_mul_f32 v[36:37], v[38:39], v[86:87]
	v_bfe_u32 v38, v90, 16, 1
	v_bfe_u32 v39, v88, 16, 1
	v_add3_u32 v39, v88, v39, s76
	v_add3_u32 v38, v90, v38, s76
	s_nop 1
	v_bfe_u32 v88, v122, 16, 1
	v_bfe_u32 v90, v124, 16, 1
	v_cmp_lt_i32_e32 vcc, -1, v97
	v_add3_u32 v90, v124, v90, s76
	v_add3_u32 v88, v122, v88, s76
	s_nop 1
	v_cndmask_b32_e32 v36, 0, v36, vcc
	v_cmp_lt_i32_e32 vcc, -1, v110
	s_nop 2
	v_lshrrev_b32_e32 v88, 16, v88
	v_lshrrev_b32_e32 v90, 16, v90
	v_cndmask_b32_e32 v37, 0, v37, vcc
	v_and_or_b32 v231, v38, s75, v90
	v_and_or_b32 v230, v39, s75, v88
	v_cvt_pk_bf16_f32 v233, v127, v109
	v_cvt_pk_bf16_f32 v232, v99, v108
	v_bfe_u32 v84, v96, 16, 1
	v_bfe_u32 v38, v37, 16, 1
	v_add3_u32 v84, v96, v84, s76
	s_waitcnt vmcnt(3)
	v_mfma_f32_16x16x32_bf16 v[96:99], v[100:103], v[230:233], v[12:15]
	v_bfe_u32 v39, v36, 16, 1
	v_bfe_u32 v85, v91, 16, 1
	v_add3_u32 v37, v37, v38, s76
	v_add_co_u32_e32 v12, vcc, s4, v178
	v_bfe_u32 v38, v89, 16, 1
	s_nop 0
	v_addc_co_u32_e32 v13, vcc, 0, v179, vcc
	s_mov_b32 s4, 0x300000
	v_add3_u32 v85, v91, v85, s76
	v_add3_u32 v36, v36, v39, s76
	v_bfe_u32 v39, v121, 16, 1
	v_add3_u32 v38, v89, v38, s76
	s_waitcnt vmcnt(2)
	v_mfma_f32_16x16x32_bf16 v[88:91], v[104:107], v[230:233], v[4:7]
	v_add3_u32 v39, v121, v39, s76
	global_load_dwordx4 v[120:123], v[12:13], off
	v_bfe_u32 v86, v71, 16, 1
	v_add_co_u32_e32 v4, vcc, s4, v178
	v_bfe_u32 v87, v70, 16, 1
	s_nop 0
	v_addc_co_u32_e32 v5, vcc, 0, v179, vcc
	global_load_dwordx4 v[124:127], v[4:5], off
	v_add_co_u32_e32 v6, vcc, s6, v68
	v_lshl_add_u64 v[4:5], v[68:69], 0, s[10:11]
	s_nop 0
	v_addc_co_u32_e32 v7, vcc, 0, v69, vcc
	global_load_dwordx4 v[172:175], v[246:247], off offset:1088
	global_load_dwordx4 v[168:171], v[246:247], off offset:2112
	global_load_dwordx4 v[180:183], v[246:247], off offset:64
	global_load_dwordx4 v[176:179], v[246:247], off offset:3136
	v_add3_u32 v70, v70, v87, s76
	v_add3_u32 v71, v71, v86, s76
	v_lshrrev_b32_e32 v38, 16, v38
	v_lshrrev_b32_e32 v39, 16, v39
	v_lshrrev_b32_e32 v71, 16, v71
	v_lshrrev_b32_e32 v70, 16, v70
	v_and_or_b32 v237, v37, s75, v70
	v_and_or_b32 v236, v36, s75, v71
	v_and_or_b32 v235, v84, s75, v39
	v_and_or_b32 v234, v85, s75, v38
	v_readlane_b32 s4, v251, 34
	v_pk_mul_f32 v[32:33], v[204:205], v[32:33] op_sel_hi:[0,1]
	v_mfma_f32_16x16x32_bf16 v[36:39], v[92:95], v[234:237], v[28:31]
	v_mul_f32_e64 v10, v206, v10
	v_mul_f32_e64 v11, v206, v11
	v_pk_mul_f32 v[8:9], v[206:207], v[8:9] op_sel_hi:[0,1]
	v_pk_mul_f32 v[6:7], v[206:207], v[150:151] op_sel_hi:[0,1]
	v_mfma_f32_16x16x32_bf16 v[28:31], v[104:107], v[234:237], v[0:3]
	v_mul_f32_e64 v4, v206, v148
	v_mul_f32_e64 v5, v206, v149
	v_readlane_b32 s5, v251, 35
	s_andn2_b64 vcc, exec, s[4:5]
	v_pk_mul_f32 v[2:3], v[204:205], v[18:19] op_sel_hi:[0,1]
	v_pk_mul_f32 v[0:1], v[204:205], v[16:17] op_sel_hi:[0,1]
	v_mfma_f32_16x16x32_bf16 v[108:111], v[92:95], v[230:233], v[32:35]
	s_waitcnt vmcnt(7)
; __device__ __forceinline__ f32x4 mfma16(bf16x8 a, bf16x8 b, f32x4 c) { return __builtin_amdgcn_mfma_f32_16x16x32_bf16(a, b, c, 0, 0, 0); }
; __device__ __forceinline__ void ret_task(const Frame& F, int l, int task) {
;     ...
;             for (int eb = 0; eb < 8; ++eb)
; #pragma unroll
;                 for (int qb = 0; qb < 2; ++qb) acc[qb][eb] = mfma16(Vf[eb], Pf[qb], acc[qb][eb]);
;         }
;         if (g == 0) {
;             if (qb2) {
; #pragma unroll
;                 for (int eb = 0; eb < 8; ++eb) Vf[eb] = ld_b8(SWP + (size_t)(SW_VR + h * HD + eb * 16 + c) * SWPP + tc0 + 32 + 8 * rq);
;             }
; #pragma unroll
;             for (int eb = 0; eb < 8; ++eb) { const int e0 = h * HD + eb * 16 + rq * 4;
; #pragma unroll
;                 for (int qb = 0; qb < 2; ++qb) gwq[qb][eb] = ld_u2(TOK + (size_t)(tq0 + qb * 16 + c) * TOKP + TK_GR + e0); }
;         }
	v_mfma_f32_16x16x32_bf16 v[84:87], v[112:115], v[230:233], v[0:3]
	s_nop 2
	v_mul_f32_e64 v2, v206, v42
	v_mul_f32_e64 v3, v206, v43
	v_pk_mul_f32 v[0:1], v[206:207], v[40:41] op_sel_hi:[0,1]
	v_mfma_f32_16x16x32_bf16 v[32:35], v[100:103], v[234:237], v[8:11]
	v_mul_f32_e64 v42, v204, v162
	v_mul_f32_e64 v43, v204, v163
	v_pk_mul_f32 v[40:41], v[204:205], v[160:161] op_sel_hi:[0,1]
	v_mfma_f32_16x16x32_bf16 v[16:19], v[112:115], v[234:237], v[0:3]
	s_nop 2
	v_mul_f32_e64 v2, v204, v46
	v_mul_f32_e64 v3, v204, v47
	v_pk_mul_f32 v[0:1], v[204:205], v[44:45] op_sel_hi:[0,1]
	s_waitcnt vmcnt(5)
	v_mfma_f32_16x16x32_bf16 v[8:11], v[120:123], v[234:237], v[4:7]
	v_mfma_f32_16x16x32_bf16 v[68:71], v[116:119], v[230:233], v[0:3]
	s_nop 2
	v_mul_f32_e64 v2, v206, v50
	v_mul_f32_e64 v3, v206, v51
	v_pk_mul_f32 v[0:1], v[206:207], v[48:49] op_sel_hi:[0,1]
	v_mfma_f32_16x16x32_bf16 v[40:43], v[76:79], v[230:233], v[40:43]
	s_nop 0
	v_mfma_f32_16x16x32_bf16 v[12:15], v[116:119], v[234:237], v[0:3]
	s_nop 2
	v_mul_f32_e64 v2, v204, v146
	v_mul_f32_e64 v3, v204, v147
	v_pk_mul_f32 v[0:1], v[204:205], v[144:145] op_sel_hi:[0,1]
	v_pk_mul_f32 v[146:147], v[206:207], v[166:167] op_sel_hi:[0,1]
	v_pk_mul_f32 v[144:145], v[206:207], v[164:165] op_sel_hi:[0,1]
	v_mfma_f32_16x16x32_bf16 v[48:51], v[120:123], v[230:233], v[0:3]
	s_nop 2
	v_mul_f32_e64 v2, v204, v154
	v_mul_f32_e64 v3, v204, v155
	v_pk_mul_f32 v[0:1], v[204:205], v[152:153] op_sel_hi:[0,1]
	s_waitcnt vmcnt(4)
	s_nop 0
	v_mfma_f32_16x16x32_bf16 v[44:47], v[124:127], v[230:233], v[0:3]
	s_nop 2
	v_mul_f32_e64 v2, v206, v158
	v_mul_f32_e64 v3, v206, v159
	v_pk_mul_f32 v[0:1], v[206:207], v[156:157] op_sel_hi:[0,1]
	s_nop 1
	v_mfma_f32_16x16x32_bf16 v[4:7], v[124:127], v[234:237], v[0:3]
	s_nop 2
	v_cndmask_b32_e64 v0, 0, 1, s[4:5]
	v_cmp_ne_u32_e64 s[34:35], 1, v0
	v_mfma_f32_16x16x32_bf16 v[0:3], v[76:79], v[234:237], v[144:147]
	s_cbranch_vccnz .LBB0_657
	s_lshl_b64 s[0:1], s[0:1], 1
	s_add_u32 s0, s64, s0
	s_addc_u32 s1, s65, s1
	v_lshl_add_u64 v[76:77], s[0:1], 0, v[184:185]
	v_lshl_add_u64 v[76:77], v[202:203], 1, v[76:77]
	v_mov_b32_e32 v76, v238
	v_mov_b32_e32 v77, v239
	v_add_co_u32_e32 v78, vcc, 0, v76
	s_nop 1
	v_addc_co_u32_e32 v79, vcc, 0, v77, vcc
	v_add_co_u32_e32 v100, vcc, 0x80000, v76
	s_nop 1
	v_addc_co_u32_e32 v101, vcc, 0, v77, vcc
	global_load_dwordx4 v[92:95], v[78:79], off offset:1024
	s_nop 0
	global_load_dwordx4 v[100:103], v[100:101], off offset:1024
	v_add_co_u32_e32 v78, vcc, 0x100000, v76
	s_nop 1
	v_addc_co_u32_e32 v79, vcc, 0, v77, vcc
	v_add_co_u32_e32 v112, vcc, 0x180000, v76
	s_nop 1
	v_addc_co_u32_e32 v113, vcc, 0, v77, vcc
	global_load_dwordx4 v[104:107], v[78:79], off offset:1024
	s_nop 0
	global_load_dwordx4 v[112:115], v[112:113], off offset:1024
	v_add_co_u32_e32 v78, vcc, 0x200000, v76
	s_nop 1
	v_addc_co_u32_e32 v79, vcc, 0, v77, vcc
	v_add_co_u32_e32 v120, vcc, 0x280000, v76
	s_nop 1
	v_addc_co_u32_e32 v121, vcc, 0, v77, vcc
	global_load_dwordx4 v[116:119], v[78:79], off offset:1024
	s_nop 0
	global_load_dwordx4 v[120:123], v[120:121], off offset:1024
	v_add_co_u32_e32 v78, vcc, 0x300000, v76
	s_nop 1
	v_addc_co_u32_e32 v79, vcc, 0, v77, vcc
	v_add_co_u32_e32 v76, vcc, 0x380000, v76
	s_nop 1
	v_addc_co_u32_e32 v77, vcc, 0, v77, vcc
	global_load_dwordx4 v[124:127], v[78:79], off offset:1024
	s_nop 0
	global_load_dwordx4 v[76:79], v[76:77], off offset:1024
.LBB0_657:
	v_lshlrev_b32_e32 v208, 2, v205
	s_nop 0
	v_add_u32_e32 v144, s9, v208
	v_ashrrev_i32_e32 v145, 31, v144
	v_lshlrev_b64 v[156:157], 1, v[144:145]
	v_lshl_add_u64 v[144:145], v[198:199], 0, v[156:157]
	s_mov_b64 s[0:1], 0x2000
	v_lshl_add_u64 v[146:147], v[144:145], 0, s[0:1]
	v_add_co_u32_e32 v144, vcc, 0x2000, v144
	v_lshl_add_u64 v[148:149], v[200:201], 0, v[156:157]
	s_nop 0
	v_addc_co_u32_e32 v145, vcc, 0, v145, vcc
	v_lshl_add_u64 v[230:231], v[148:149], 0, s[0:1]
	v_add_co_u32_e32 v148, vcc, 0x2000, v148
	s_movk_i32 s33, 0x1100
	s_nop 0
	v_addc_co_u32_e32 v149, vcc, 0, v149, vcc
	v_mov_b32_e32 v242, 0x8000
	v_mov_b32_e32 v243, 0
	v_lshl_add_u64 v[242:243], v[248:249], 0, v[242:243]
	global_load_dwordx2 v[204:205], v[248:249], off offset:512
	global_load_dwordx2 v[202:203], v[248:249], off offset:1024
	global_load_dwordx2 v[200:201], v[248:249], off offset:1536
	global_load_dwordx2 v[198:199], v[248:249], off offset:2048
	global_load_dwordx2 v[158:159], v[242:243], off offset:512
	global_load_dwordx2 v[154:155], v[242:243], off offset:1024
	global_load_dwordx2 v[152:153], v[242:243], off offset:1536
	global_load_dwordx2 v[150:151], v[242:243], off offset:2048
	global_load_dwordx2 v[206:207], v[248:249], off
	global_load_dwordx2 v[166:167], v[248:249], off offset:2560
	global_load_dwordx2 v[164:165], v[248:249], off offset:3072
	global_load_dwordx2 v[162:163], v[248:249], off offset:3584
	global_load_dwordx2 v[160:161], v[242:243], off
	s_nop 0
	global_load_dwordx2 v[148:149], v[242:243], off offset:2560
	global_load_dwordx2 v[146:147], v[242:243], off offset:3072
	global_load_dwordx2 v[144:145], v[242:243], off offset:3584
	s_and_b64 vcc, exec, s[34:35]
	s_cbranch_vccnz .LBB0_633
; __device__ __forceinline__ f32x4 mfma16(bf16x8 a, bf16x8 b, f32x4 c) { return __builtin_amdgcn_mfma_f32_16x16x32_bf16(a, b, c, 0, 0, 0); }
; __device__ __forceinline__ float fexp2(float x) { return __builtin_amdgcn_exp2f(x); }
; __device__ __forceinline__ void ret_task(const Frame& F, int l, int task) {
;     ...
;     for (int g = 0; g < 2; ++g) {
;         if (g <= qb2) {
;             f32x4 sa[2][2];
; #pragma unroll
;             for (int qb = 0; qb < 2; ++qb)
; #pragma unroll
;                 for (int ab = 0; ab < 2; ++ab) sa[qb][ab] = (f32x4){0.f, 0.f, 0.f, 0.f};
; #pragma unroll
;             for (int ab = 0; ab < 2; ++ab)
; #pragma unroll
;                 for (int ks = 0; ks < 4; ++ks)
; #pragma unroll
;                     for (int qb = 0; qb < 2; ++qb) sa[qb][ab] = mfma16(Kf[g][ab][ks], Qf[qb][ks], sa[qb][ab]);
;             bf16x8 Pf[2];
; #pragma unroll
;             for (int qb = 0; qb < 2; ++qb) {
;                 const int i = qb2 * 32 + qb * 16 + c;
; #pragma unroll
;                 for (int ab = 0; ab < 2; ++ab)
; #pragma unroll
;                     for (int e = 0; e < 4; ++e) { const int diff = i - (32 * g + 8 * rq + 4 * ab + e);
;                         sa[qb][ab][e] = diff >= 0 ? sa[qb][ab][e] * fexp2((float)diff * lg) : 0.f; }
;                 Pf[qb] = pack8(sa[qb][0], sa[qb][1]);
	v_mfma_f32_16x16x32_bf16 v[230:233], v[140:143], v[20:23], 0
	s_waitcnt vmcnt(17)
	v_mfma_f32_16x16x32_bf16 v[20:23], v[180:183], v[20:23], 0
	v_mfma_f32_16x16x32_bf16 v[140:143], v[140:143], v[24:27], 0
	v_mfma_f32_16x16x32_bf16 v[24:27], v[180:183], v[24:27], 0
	v_mfma_f32_16x16x32_bf16 v[230:233], v[132:135], v[52:55], v[230:233]
	v_mfma_f32_16x16x32_bf16 v[20:23], v[172:175], v[52:55], v[20:23]
	v_mfma_f32_16x16x32_bf16 v[24:27], v[172:175], v[56:59], v[24:27]
	v_mfma_f32_16x16x32_bf16 v[132:135], v[132:135], v[56:59], v[140:143]
	v_add_u32_e32 v58, 32, v210
	v_add_u32_e32 v59, 34, v195
	v_mfma_f32_16x16x32_bf16 v[140:143], v[128:131], v[60:63], v[230:233]
	v_mfma_f32_16x16x32_bf16 v[20:23], v[168:171], v[60:63], v[20:23]
	v_add_u32_e32 v60, 33, v210
	v_add_u32_e32 v61, 35, v195
	v_add_u32_e32 v62, 36, v210
	v_mfma_f32_16x16x32_bf16 v[52:55], v[168:171], v[64:67], v[24:27]
	v_add_u32_e32 v63, 38, v195
	v_mfma_f32_16x16x32_bf16 v[128:131], v[128:131], v[64:67], v[132:135]
	v_sub_u32_e32 v66, v209, v58
	v_sub_u32_e32 v67, v209, v61
	v_add_u32_e32 v64, 37, v210
	v_mfma_f32_16x16x32_bf16 v[132:135], v[136:139], v[72:75], v[140:143]
	v_add_u32_e32 v65, 39, v195
	v_sub_u32_e32 v58, v228, v58
	s_waitcnt vmcnt(16)
; __device__ __forceinline__ f32x4 mfma16(bf16x8 a, bf16x8 b, f32x4 c) { return __builtin_amdgcn_mfma_f32_16x16x32_bf16(a, b, c, 0, 0, 0); }
; __device__ __forceinline__ float fexp2(float x) { return __builtin_amdgcn_exp2f(x); }
; __device__ __forceinline__ void ret_task(const Frame& F, int l, int task) {
;     ...
;             for (int ab = 0; ab < 2; ++ab)
; #pragma unroll
;                 for (int ks = 0; ks < 4; ++ks)
; #pragma unroll
;                     for (int qb = 0; qb < 2; ++qb) sa[qb][ab] = mfma16(Kf[g][ab][ks], Qf[qb][ks], sa[qb][ab]);
;             bf16x8 Pf[2];
; #pragma unroll
;             for (int qb = 0; qb < 2; ++qb) {
;                 const int i = qb2 * 32 + qb * 16 + c;
; #pragma unroll
;                 for (int ab = 0; ab < 2; ++ab)
; #pragma unroll
;                     for (int e = 0; e < 4; ++e) { const int diff = i - (32 * g + 8 * rq + 4 * ab + e);
;                         sa[qb][ab][e] = diff >= 0 ? sa[qb][ab][e] * fexp2((float)diff * lg) : 0.f; }
;                 Pf[qb] = pack8(sa[qb][0], sa[qb][1]);
;             }
; #pragma unroll
;             for (int eb = 0; eb < 8; ++eb)
; #pragma unroll
;                 for (int qb = 0; qb < 2; ++qb) acc[qb][eb] = mfma16(Vf[eb], Pf[qb], acc[qb][eb]);
	v_mfma_f32_16x16x32_bf16 v[24:27], v[176:179], v[72:75], v[20:23]
	v_sub_u32_e32 v72, v209, v60
	s_nop 2
	v_mov_b32_e32 v56, v132
	v_mov_b32_e32 v57, v134
	v_mfma_f32_16x16x32_bf16 v[20:23], v[176:179], v[80:83], v[52:55]
	v_mov_b32_e32 v134, v133
	v_sub_u32_e32 v74, v209, v62
	v_sub_u32_e32 v75, v209, v65
	v_cvt_f32_u32_e32 v53, v72
	v_sub_u32_e32 v55, v209, v59
	v_cvt_f32_u32_e32 v52, v66
	v_cmp_lt_i32_e32 vcc, -1, v55
	v_mul_f32_e32 v53, v197, v53
	v_exp_f32_e32 v54, v53
	v_cvt_f32_u32_e32 v53, v55
	v_mul_f32_e32 v52, v197, v52
	v_exp_f32_e32 v52, v52
	v_mfma_f32_16x16x32_bf16 v[128:131], v[136:139], v[80:83], v[128:131]
	v_mul_f32_e32 v53, v197, v53
	v_exp_f32_e32 v53, v53
	v_sub_u32_e32 v80, v209, v64
	v_sub_u32_e32 v60, v228, v60
	v_sub_u32_e32 v64, v228, v64
	v_pk_mul_f32 v[52:53], v[52:53], v[56:57]
	v_mov_b32_e32 v56, v24
	v_cndmask_b32_e32 v73, 0, v53, vcc
	v_cmp_lt_i32_e32 vcc, -1, v66
	v_cvt_f32_u32_e32 v24, v75
	v_mov_b32_e32 v57, v26
	v_cndmask_b32_e32 v66, 0, v52, vcc
	v_cvt_f32_u32_e32 v52, v67
	v_cmp_lt_i32_e32 vcc, -1, v72
	v_mul_f32_e32 v24, v197, v24
	v_mov_b32_e32 v26, v25
	v_mul_f32_e32 v52, v197, v52
	v_exp_f32_e32 v55, v52
	v_sub_u32_e32 v62, v228, v62
	v_pk_mul_f32 v[52:53], v[54:55], v[134:135]
	s_nop 0
	v_cndmask_b32_e32 v72, 0, v52, vcc
	v_cmp_lt_i32_e32 vcc, -1, v67
	v_sub_u32_e32 v55, v209, v63
	v_cvt_f32_u32_e32 v52, v74
	v_cndmask_b32_e32 v67, 0, v53, vcc
	v_cvt_f32_u32_e32 v53, v80
	v_cmp_lt_i32_e32 vcc, -1, v55
	v_mul_f32_e32 v52, v197, v52
	v_exp_f32_e32 v52, v52
	v_mul_f32_e32 v53, v197, v53
	v_exp_f32_e32 v54, v53
	v_cvt_f32_u32_e32 v53, v55
	v_exp_f32_e32 v55, v24
	v_mul_f32_e32 v53, v197, v53
	v_exp_f32_e32 v53, v53
	v_pk_mul_f32 v[24:25], v[54:55], v[26:27]
	s_nop 1
	v_pk_mul_f32 v[52:53], v[52:53], v[56:57]
	s_nop 0
	v_cndmask_b32_e32 v53, 0, v53, vcc
	v_cmp_lt_i32_e32 vcc, -1, v74
	v_bfe_u32 v57, v53, 16, 1
	v_add3_u32 v53, v53, v57, s76
	v_cndmask_b32_e32 v52, 0, v52, vcc
	v_cmp_lt_i32_e32 vcc, -1, v80
	v_bfe_u32 v56, v52, 16, 1
	v_add3_u32 v52, v52, v56, s76
	v_cndmask_b32_e32 v24, 0, v24, vcc
	v_bfe_u32 v27, v24, 16, 1
	v_cmp_lt_i32_e32 vcc, -1, v75
	v_add3_u32 v24, v24, v27, s76
	s_nop 0
	v_cndmask_b32_e32 v25, 0, v25, vcc
	s_nop 0
	v_bfe_u32 v26, v25, 16, 1
	s_nop 0
	v_lshrrev_b32_e32 v27, 16, v53
	v_cvt_f32_u32_e32 v53, v60
	v_add3_u32 v25, v25, v26, s76
	s_nop 2
	v_lshrrev_b32_e32 v26, 16, v52
	s_nop 0
	v_and_or_b32 v26, v24, s75, v26
	v_cvt_pk_bf16_f32 v24, v66, v72
	v_sub_u32_e32 v55, v228, v59
	v_mul_f32_e32 v53, v197, v53
	v_and_or_b32 v27, v25, s75, v27
	v_cvt_pk_bf16_f32 v25, v73, v67
	v_cvt_f32_u32_e32 v52, v58
	v_exp_f32_e32 v54, v53
	v_cvt_f32_u32_e32 v53, v55
	v_mov_b32_e32 v56, v128
	v_mul_f32_e32 v52, v197, v52
	v_exp_f32_e32 v52, v52
	v_mul_f32_e32 v53, v197, v53
	v_exp_f32_e32 v53, v53
	v_mov_b32_e32 v57, v130
	v_cmp_lt_i32_e32 vcc, -1, v55
	v_sub_u32_e32 v59, v228, v61
	v_pk_mul_f32 v[52:53], v[52:53], v[56:57]
	v_mov_b32_e32 v130, v129
	v_cndmask_b32_e32 v61, 0, v53, vcc
	v_cmp_lt_i32_e32 vcc, -1, v58
	v_mov_b32_e32 v56, v20
	v_mov_b32_e32 v57, v22
	v_cndmask_b32_e32 v58, 0, v52, vcc
	v_cvt_f32_u32_e32 v52, v59
	v_cmp_lt_i32_e32 vcc, -1, v60
	v_mov_b32_e32 v22, v21
	v_mfma_f32_16x16x32_bf16 v[108:111], v[92:95], v[24:27], v[108:111]
	v_mul_f32_e32 v52, v197, v52
	v_exp_f32_e32 v55, v52
	v_mfma_f32_16x16x32_bf16 v[96:99], v[100:103], v[24:27], v[96:99]
	v_mul_f32_e64 v52, v54, v130
	v_mul_f32_e64 v53, v55, v131
	v_cndmask_b32_e32 v60, 0, v52, vcc
	v_cmp_lt_i32_e32 vcc, -1, v59
	v_sub_u32_e32 v55, v228, v63
	v_cvt_f32_u32_e32 v52, v62
	v_cndmask_b32_e32 v59, 0, v53, vcc
	v_cvt_f32_u32_e32 v53, v64
	v_sub_u32_e32 v63, v228, v65
	v_cvt_f32_u32_e32 v20, v63
	v_mul_f32_e32 v52, v197, v52
	v_mul_f32_e32 v53, v197, v53
	v_exp_f32_e32 v54, v53
	v_cvt_f32_u32_e32 v53, v55
	v_exp_f32_e32 v52, v52
	v_mul_f32_e32 v20, v197, v20
	v_cmp_lt_i32_e32 vcc, -1, v55
	v_mul_f32_e32 v53, v197, v53
	v_exp_f32_e32 v53, v53
	v_exp_f32_e32 v55, v20
	v_mfma_f32_16x16x32_bf16 v[88:91], v[104:107], v[24:27], v[88:91]
	v_mul_f32_e64 v52, v52, v56
	v_mul_f32_e64 v53, v53, v57
	v_cndmask_b32_e32 v53, 0, v53, vcc
	v_cmp_lt_i32_e32 vcc, -1, v62
	v_pk_mul_f32 v[20:21], v[54:55], v[22:23]
	v_bfe_u32 v57, v53, 16, 1
	v_cndmask_b32_e32 v52, 0, v52, vcc
	v_cmp_lt_i32_e32 vcc, -1, v64
	v_bfe_u32 v56, v52, 16, 1
	v_bfe_u32 v54, v59, 16, 1
	v_cndmask_b32_e32 v20, 0, v20, vcc
	v_cmp_lt_i32_e32 vcc, -1, v63
	v_bfe_u32 v23, v20, 16, 1
	v_add3_u32 v20, v20, v23, s76
	v_cndmask_b32_e32 v21, 0, v21, vcc
	v_bfe_u32 v22, v21, 16, 1
	v_add3_u32 v21, v21, v22, s76
	v_bfe_u32 v22, v58, 16, 1
	v_bfe_u32 v23, v61, 16, 1
	v_bfe_u32 v55, v60, 16, 1
	v_add3_u32 v53, v53, v57, s76
	v_add3_u32 v52, v52, v56, s76
	v_add3_u32 v23, v61, v23, s76
	v_add3_u32 v22, v58, v22, s76
	v_add3_u32 v55, v60, v55, s76
	v_add3_u32 v54, v59, v54, s76
	v_lshrrev_b32_e32 v56, 16, v22
	v_lshrrev_b32_e32 v57, 16, v23
	v_lshrrev_b32_e32 v22, 16, v52
	v_lshrrev_b32_e32 v23, 16, v53
	v_and_or_b32 v23, v21, s75, v23
	v_and_or_b32 v22, v20, s75, v22
	v_cvt_pk_bf16_f32 v21, v61, v59
	v_cvt_pk_bf16_f32 v20, v58, v60
	v_mfma_f32_16x16x32_bf16 v[84:87], v[112:115], v[24:27], v[84:87]
	s_nop 0
	v_mfma_f32_16x16x32_bf16 v[36:39], v[92:95], v[20:23], v[36:39]
	v_mfma_f32_16x16x32_bf16 v[32:35], v[100:103], v[20:23], v[32:35]
	v_mfma_f32_16x16x32_bf16 v[28:31], v[104:107], v[20:23], v[28:31]
	v_mfma_f32_16x16x32_bf16 v[16:19], v[112:115], v[20:23], v[16:19]
	v_mfma_f32_16x16x32_bf16 v[68:71], v[116:119], v[24:27], v[68:71]
	v_mfma_f32_16x16x32_bf16 v[12:15], v[116:119], v[20:23], v[12:15]
	v_mfma_f32_16x16x32_bf16 v[48:51], v[120:123], v[24:27], v[48:51]
	v_mfma_f32_16x16x32_bf16 v[8:11], v[120:123], v[20:23], v[8:11]
	v_mfma_f32_16x16x32_bf16 v[44:47], v[124:127], v[24:27], v[44:47]
	v_mfma_f32_16x16x32_bf16 v[4:7], v[124:127], v[20:23], v[4:7]
	v_mfma_f32_16x16x32_bf16 v[40:43], v[76:79], v[24:27], v[40:43]
	v_mfma_f32_16x16x32_bf16 v[0:3], v[76:79], v[20:23], v[0:3]
	s_branch .LBB0_633
